# speedup vs baseline: 1.0093x; 1.0028x over previous
_Z9qsim_mainPKDF16_PK15HIP_vector_typeIfLj2EEPf:
	s_cmpk_gt_i32 s2, 0x3ff
	s_cbranch_scc1 .LBB1_11
	s_load_dwordx4 s[8:11], s[0:1], 0x0
	s_load_dwordx2 s[4:5], s[0:1], 0x10
	s_mul_i32 s1, s2, 56
	s_mul_hi_i32 s0, s2, 56
	v_mbcnt_lo_u32_b32 v2, -1, 0
	s_waitcnt lgkmcnt(0)
	s_add_u32 s6, s8, 0x20000
	s_addc_u32 s7, s9, 0
	s_add_u32 s20, s8, 0x80000
	s_addc_u32 s21, s9, 0
	s_add_u32 s12, s8, 0x38000
	s_addc_u32 s13, s9, 0
	s_add_i32 s22, s2, 0xfffffe00
	s_add_u32 s14, s4, s1
	s_addc_u32 s15, s5, s0
	s_mul_hi_i32 s0, s2, 0xa00
	s_mulk_i32 s2, 0xa00
	v_mbcnt_hi_u32_b32 v161, -1, v2
	s_add_u32 s10, s10, s2
	v_and_b32_e32 v2, 64, v161
	s_addc_u32 s11, s11, s0
	v_mov_b32_e32 v155, 0
	s_movk_i32 s23, 0x1000
	s_mov_b64 s[16:17], 0x28000
	v_mov_b32_e32 v1, 0x10000
	s_movk_i32 s24, 0x100
	v_mov_b32_e32 v158, 0x60
	v_mov_b32_e32 v159, 0x280
	v_mov_b32_e32 v160, 0x1280
	s_mov_b64 s[18:19], 0x40000
	s_mov_b32 s25, 0x40000
	v_xor_b32_e32 v162, 32, v161
	v_add_u32_e32 v163, 64, v2
	v_xor_b32_e32 v164, 16, v161
	v_mov_b32_e32 v165, 0x10a00
	v_and_b32_e32 v2, 63, v0
	v_lshlrev_b32_e32 v2, 4, v2
	v_add_u32_e32 v3, 0x1000, v2
	global_load_dwordx4 v[222:225], v2, s[6:7]
	global_load_dwordx4 v[226:229], v2, s[6:7] offset:1024
	global_load_dwordx4 v[230:233], v2, s[6:7] offset:2048
	global_load_dwordx4 v[234:237], v2, s[6:7] offset:3072
	global_load_dwordx4 v[238:241], v3, s[6:7]
	global_load_dwordx4 v[242:245], v3, s[6:7] offset:1024
	global_load_dwordx4 v[246:249], v3, s[6:7] offset:2048
	global_load_dwordx4 v[250:253], v3, s[6:7] offset:3072
	s_nop 0
	s_nop 0
	s_branch .LBB1_3

.LBB1_3:
	v_mov_b32_e32 v156, v0
	s_nop 0
	v_ashrrev_i32_e32 v157, 31, v156
	v_and_b32_e32 v167, 63, v156
	v_lshl_add_u64 v[6:7], v[156:157], 3, s[10:11]
	v_lshlrev_b32_e32 v169, 3, v167
	global_load_dwordx2 v[4:5], v[6:7], off
	global_load_dwordx2 v[2:3], v169, s[10:11] offset:2048
	v_readfirstlane_b32 s4, v156
	s_ashr_i32 s27, s4, 7
	s_lshl_b32 s0, s27, 1
	s_ashr_i32 s1, s0, 31
	s_lshl_b64 s[2:3], s[0:1], 13
	s_add_u32 s2, s8, s2
	s_addc_u32 s3, s9, s3
	s_add_u32 s28, s2, 0x18000
	s_addc_u32 s29, s3, 0
	v_lshlrev_b32_e32 v154, 4, v167
	v_lshl_add_u64 v[6:7], s[28:29], 0, v[154:155]
	v_or_b32_e32 v8, 0x800, v169
	v_add_co_u32_e32 v6, vcc, s23, v6
	v_lshlrev_b32_e32 v168, 1, v8
	s_nop 0
	v_addc_co_u32_e32 v7, vcc, 0, v7, vcc
	global_load_dwordx4 v[150:153], v154, s[28:29]
	global_load_dwordx4 v[146:149], v154, s[28:29] offset:1024
	global_load_dwordx4 v[142:145], v154, s[28:29] offset:2048
	global_load_dwordx4 v[138:141], v154, s[28:29] offset:3072
	global_load_dwordx4 v[126:129], v[6:7], off offset:1024
	global_load_dwordx4 v[122:125], v[6:7], off offset:2048
	global_load_dwordx4 v[134:137], v168, s[28:29]
	global_load_dwordx4 v[130:133], v[6:7], off offset:3072
	v_lshl_add_u64 v[6:7], s[2:3], 0, v[154:155]
	v_lshl_add_u64 v[8:9], v[6:7], 0, s[16:17]
	v_add_co_u32_e32 v6, vcc, 0x28000, v6
	s_nop 1
	v_addc_co_u32_e32 v7, vcc, 0, v7, vcc
	global_load_dwordx4 v[86:89], v[6:7], off
	global_load_dwordx4 v[82:85], v[8:9], off offset:1024
	v_cmp_gt_i32_e32 vcc, 16, v156
	v_lshl_add_u32 v166, v156, 2, v165
	s_and_saveexec_b64 s[2:3], vcc
	ds_write_b32 v166, v155
	s_or_b64 exec, exec, s[2:3]
	v_lshl_add_u32 v6, v156, 3, v1
	v_cmp_gt_i32_e32 vcc, 64, v156
	s_waitcnt vmcnt(11)
	ds_write_b64 v6, v[4:5]
	s_and_saveexec_b64 s[2:3], vcc
	s_cbranch_execz .LBB1_7
	s_waitcnt vmcnt(10)
	ds_write_b64 v6, v[2:3] offset:2048
.LBB1_7:
	s_or_b64 exec, exec, s[2:3]
	v_mov_b32_e32 v10, v167
	s_waitcnt lgkmcnt(0)
	s_barrier
	s_waitcnt vmcnt(10)
	s_ashr_i32 s2, s4, 6
	s_lshl_b32 s3, s2, 3
	s_and_b32 s5, s3, 8
	s_bfe_u32 s26, s2, 0x10001
	s_or_b32 s5, s26, s5
	s_lshl_b32 s26, s2, 9
	s_and_b32 s26, s26, 0x400
	s_lshl_b32 s5, s5, 4
	s_or_b32 s28, s5, s26
	v_lshrrev_b32_e32 v182, 5, v167
	v_bfe_u32 v2, v156, 4, 1
	v_bitop3_b32 v3, v182, v156, 1 bitop3:0x78
	v_lshlrev_b32_e32 v154, 2, v182
	v_xor_b32_e32 v3, v3, v2
	v_bitop3_b32 v4, v154, v156, 4 bitop3:0x78
	v_and_b32_e32 v5, 10, v156
	v_or3_b32 v3, v5, v4, v3
	s_lshl_b32 s5, s2, 4
	v_lshlrev_b32_e32 v3, 4, v3
	s_lshl_b32 s3, s2, 13
	s_and_b32 s29, s5, 16
	v_lshlrev_b32_e32 v170, 8, v182
	v_lshl_or_b32 v171, v2, 10, v3
	s_or_b32 s26, s29, s3
	v_bitop3_b32 v179, v171, s26, v170 bitop3:0x36
	s_or_b32 s5, s26, 0x280
	v_bitop3_b32 v178, v171, s5, v170 bitop3:0x36
	s_or_b32 s30, s3, 0x800
	s_or_b32 s33, s3, 0x1000
	s_or_b32 s29, s29, 64
	s_or_b32 s34, s29, s33
	v_bitop3_b32 v180, v171, s34, v170 bitop3:0x36
	s_or_b32 s29, s3, s29
	s_or_b32 s29, s29, 0x1280
	s_and_b32 s5, s2, 1
	s_lshl_b32 s31, s5, 4
	s_or_b32 s2, s31, s3
	v_bitop3_b32 v173, v171, s2, v170 bitop3:0x36
	v_bitop3_b32 v34, v156, 31, v156 bitop3:0xc
	v_lshrrev_b32_e32 v35, 4, v34
	v_bitop3_b32 v36, v34, v182, 1 bitop3:0x6c
	v_xor_b32_e32 v36, v36, v35
	v_bitop3_b32 v34, v34, v154, 4 bitop3:0x6c
	v_bitop3_b32 v37, v156, 10, 31 bitop3:8
	v_or3_b32 v34, v37, v34, v36
	v_lshlrev_b32_e32 v35, 10, v35
	v_lshlrev_b32_e32 v34, 4, v34
	v_or3_b32 v154, v35, v34, v170
	v_bitop3_b32 v172, s2, v154, v159 bitop3:0x36
	v_bitop3_b32 v176, v171, s29, v170 bitop3:0x36
	s_or_b32 s29, s31, s30
	s_or_b32 s29, s29, 0xa0
	v_bitop3_b32 v175, v171, s29, v170 bitop3:0x36
	s_or_b32 s29, s2, 0xaa0
	s_xor_b32 s29, s29, 0x80
	v_xor_b32_e32 v174, s29, v154
	s_or_b32 s29, s26, 0x18e0
	v_bitop3_b32 v181, v171, s29, v170 bitop3:0x36
	s_or_b32 s29, s26, 0x1a60
	v_bitop3_b32 v177, v171, s29, v170 bitop3:0x36
	s_or_b32 s29, s31, 64
	s_or_b32 s3, s3, s29
	s_mov_b32 s41, s3
	s_or_b32 s29, s29, s33
	s_mov_b32 s40, s29
	s_or_b32 s3, s2, 0x18e0
	s_mov_b32 s42, s3
	s_or_b32 s2, s2, 0x1ae0
	s_xor_b32 s2, s2, 0x80
	s_mov_b32 s43, s2
	s_lshr_b32 s38, s4, 1
	v_and_b32_e32 v26, 31, v167
	v_and_b32_e32 v27, 3, v167
	v_bfe_u32 v28, v167, 3, 1
	v_bfe_u32 v29, v167, 2, 1
	v_lshl_or_b32 v27, v28, 2, v27
	v_lshl_or_b32 v27, v29, 3, v27
	v_lshlrev_b32_e32 v32, 9, v182
	v_lshl_add_u32 v30, v27, 3, v32
	v_add_u32_e32 v30, 0x10000, v30
	v_lshl_add_u32 v31, v26, 3, v32
	v_add_u32_e32 v31, 0x10400, v31
	v_xor_b32_e32 v28, 31, v26
	v_lshl_add_u32 v28, v28, 3, v32
	v_add_u32_e32 v28, 0x10400, v28
	v_bfe_u32 v29, v167, 4, 1
	v_mul_u32_u24_e32 v29, 0x78, v29
	v_xor_b32_e32 v254, s38, v29
	v_or_b32_e32 v254, 0x10800, v254
	v_and_b32_e32 v33, 16, v167
	v_cmp_eq_u32_e32 vcc, 0, v33
	ds_read2_b64 v[66:69], v30 offset0:0 offset1:32
	ds_read2_b64 v[70:73], v30 offset0:16 offset1:48
	ds_read2_b64 v[198:201], v31 offset0:0 offset1:32
	ds_read2_b64 v[202:205], v28 offset0:0 offset1:32
	ds_read2_b64 v[206:209], v254 offset0:0 offset1:16
	ds_read2_b64 v[210:213], v254 offset0:32 offset1:48
	s_waitcnt lgkmcnt(0)
	v_cndmask_b32_e32 v74, v67, v66, vcc
	v_cndmask_b32_e32 v75, v69, v68, vcc
	v_cndmask_b32_e64 v76, v66, -v67, vcc
	v_cndmask_b32_e64 v77, v68, -v69, vcc
	v_cndmask_b32_e32 v78, v71, v70, vcc
	v_cndmask_b32_e32 v79, v73, v72, vcc
	v_cndmask_b32_e64 v80, v70, -v71, vcc
	v_cndmask_b32_e64 v81, v72, -v73, vcc
	v_cvt_pk_f16_f32 v190, v74, v75
	v_cvt_pk_f16_f32 v191, v74, v75
	v_cvt_pk_f16_f32 v192, v76, v77
	v_cvt_pk_f16_f32 v193, v76, v77
	v_cvt_pk_f16_f32 v194, v78, v79
	v_cvt_pk_f16_f32 v195, v78, v79
	v_cvt_pk_f16_f32 v196, v80, v81
	v_cvt_pk_f16_f32 v197, v80, v81
	v_mul_f32_e32 v66, v199, v207
	v_mul_f32_e32 v68, v199, v206
	v_mul_f32_e32 v67, v199, v209
	v_mul_f32_e32 v69, v199, v208
	v_fma_f32 v66, v198, v206, -v66
	v_fma_f32 v68, v198, v207, v68
	v_fma_f32 v67, v198, v208, -v67
	v_fma_f32 v69, v198, v209, v69
	v_cvt_pk_f16_f32 v214, v66, v67
	v_cvt_pk_f16_f32 v216, v68, v69
	v_mul_f32_e32 v70, v201, v211
	v_mul_f32_e32 v72, v201, v210
	v_mul_f32_e32 v71, v201, v213
	v_mul_f32_e32 v73, v201, v212
	v_fma_f32 v70, v200, v210, -v70
	v_fma_f32 v72, v200, v211, v72
	v_fma_f32 v71, v200, v212, -v71
	v_fma_f32 v73, v200, v213, v73
	v_cvt_pk_f16_f32 v215, v70, v71
	v_cvt_pk_f16_f32 v217, v72, v73
	v_mul_f32_e32 v66, v203, v207
	v_mul_f32_e32 v68, v203, v206
	v_mul_f32_e32 v67, v203, v209
	v_mul_f32_e32 v69, v203, v208
	v_fma_f32 v66, v202, v206, -v66
	v_fma_f32 v68, v202, v207, v68
	v_fma_f32 v67, v202, v208, -v67
	v_fma_f32 v69, v202, v209, v69
	v_cvt_pk_f16_f32 v218, v66, v67
	v_cvt_pk_f16_f32 v220, v68, v69
	v_mul_f32_e32 v70, v205, v211
	v_mul_f32_e32 v72, v205, v210
	v_mul_f32_e32 v71, v205, v213
	v_mul_f32_e32 v73, v205, v212
	v_fma_f32 v70, v204, v210, -v70
	v_fma_f32 v72, v204, v211, v72
	v_fma_f32 v71, v204, v212, -v71
	v_fma_f32 v73, v204, v213, v73
	v_cvt_pk_f16_f32 v219, v70, v71
	v_cvt_pk_f16_f32 v221, v72, v73
	v_xor_b32_e32 v255, 8, v254
	ds_read2_b64 v[206:209], v255 offset0:0 offset1:16
	ds_read2_b64 v[210:213], v255 offset0:32 offset1:48
	v_mfma_f32_32x32x16_f16 v[2:17], v[190:193], v[214:217], 0
	v_mfma_f32_32x32x16_f16 v[18:33], v[194:197], v[218:221], 0
	s_waitcnt lgkmcnt(0)
	v_mul_f32_e32 v66, v199, v207
	v_mul_f32_e32 v68, v199, v206
	v_mul_f32_e32 v67, v199, v209
	v_mul_f32_e32 v69, v199, v208
	v_fma_f32 v66, v198, v206, -v66
	v_fma_f32 v68, v198, v207, v68
	v_fma_f32 v67, v198, v208, -v67
	v_fma_f32 v69, v198, v209, v69
	v_cvt_pk_f16_f32 v214, v66, v67
	v_cvt_pk_f16_f32 v216, v68, v69
	v_mul_f32_e32 v70, v201, v211
	v_mul_f32_e32 v72, v201, v210
	v_mul_f32_e32 v71, v201, v213
	v_mul_f32_e32 v73, v201, v212
	v_fma_f32 v70, v200, v210, -v70
	v_fma_f32 v72, v200, v211, v72
	v_fma_f32 v71, v200, v212, -v71
	v_fma_f32 v73, v200, v213, v73
	v_cvt_pk_f16_f32 v215, v70, v71
	v_cvt_pk_f16_f32 v217, v72, v73
	v_cvt_pk_f16_f32 v2, v2, v3
	v_cvt_pk_f16_f32 v3, v4, v5
	v_cvt_pk_f16_f32 v4, v6, v7
	v_cvt_pk_f16_f32 v5, v8, v9
	v_cvt_pk_f16_f32 v6, v10, v11
	v_cvt_pk_f16_f32 v7, v12, v13
	v_cvt_pk_f16_f32 v8, v14, v15
	v_cvt_pk_f16_f32 v9, v16, v17
	v_cvt_pk_f16_f32 v18, v18, v19
	v_cvt_pk_f16_f32 v19, v20, v21
	v_cvt_pk_f16_f32 v20, v22, v23
	v_cvt_pk_f16_f32 v21, v24, v25
	v_cvt_pk_f16_f32 v22, v26, v27
	v_cvt_pk_f16_f32 v23, v28, v29
	v_cvt_pk_f16_f32 v24, v30, v31
	v_cvt_pk_f16_f32 v25, v32, v33
	s_setprio 1
	s_waitcnt vmcnt(6)
	v_mul_f32_e32 v66, v203, v207
	v_mul_f32_e32 v68, v203, v206
	v_mfma_f32_32x32x16_f16 v[34:49], v[2:5], v[150:153], 0
	v_mul_f32_e32 v67, v203, v209
	v_mul_f32_e32 v69, v203, v208
	v_mfma_f32_32x32x16_f16 v[34:49], v[18:21], v[146:149], v[34:49]
	v_fma_f32 v66, v202, v206, -v66
	v_fma_f32 v68, v202, v207, v68
	v_mfma_f32_32x32x16_f16 v[34:49], v[6:9], v[142:145], v[34:49]
	v_fma_f32 v67, v202, v208, -v67
	v_fma_f32 v69, v202, v209, v69
	v_mfma_f32_32x32x16_f16 v[34:49], v[22:25], v[138:141], v[34:49]
	v_cvt_pk_f16_f32 v218, v66, v67
	v_cvt_pk_f16_f32 v220, v68, v69
	s_waitcnt vmcnt(2)
	v_mul_f32_e32 v70, v205, v211
	v_mul_f32_e32 v72, v205, v210
	v_mfma_f32_32x32x16_f16 v[50:65], v[2:5], v[134:137], 0
	v_mul_f32_e32 v71, v205, v213
	v_mul_f32_e32 v73, v205, v212
	v_mfma_f32_32x32x16_f16 v[50:65], v[18:21], v[126:129], v[50:65]
	v_fma_f32 v70, v204, v210, -v70
	v_fma_f32 v72, v204, v211, v72
	v_mfma_f32_32x32x16_f16 v[50:65], v[6:9], v[122:125], v[50:65]
	v_fma_f32 v71, v204, v212, -v71
	v_fma_f32 v73, v204, v213, v73
	v_mfma_f32_32x32x16_f16 v[50:65], v[22:25], v[130:133], v[50:65]
	v_cvt_pk_f16_f32 v219, v70, v71
	v_cvt_pk_f16_f32 v221, v72, v73
	v_xor_b32_e32 v255, 16, v254
	ds_read2_b64 v[206:209], v255 offset0:0 offset1:16
	ds_read2_b64 v[210:213], v255 offset0:32 offset1:48
	v_mfma_f32_32x32x16_f16 v[2:17], v[190:193], v[214:217], 0
	v_mfma_f32_32x32x16_f16 v[18:33], v[194:197], v[218:221], 0
	v_cvt_pk_f16_f32 v34, v34, v35
	v_cvt_pk_f16_f32 v35, v36, v37
	v_cvt_pk_f16_f32 v36, v38, v39
	v_cvt_pk_f16_f32 v37, v40, v41
	v_cvt_pk_f16_f32 v38, v42, v43
	v_cvt_pk_f16_f32 v39, v44, v45
	v_cvt_pk_f16_f32 v40, v46, v47
	v_cvt_pk_f16_f32 v41, v48, v49
	v_cvt_pk_f16_f32 v50, v50, v51
	v_cvt_pk_f16_f32 v51, v52, v53
	v_cvt_pk_f16_f32 v52, v54, v55
	v_cvt_pk_f16_f32 v53, v56, v57
	v_cvt_pk_f16_f32 v54, v58, v59
	v_cvt_pk_f16_f32 v55, v60, v61
	v_cvt_pk_f16_f32 v56, v62, v63
	v_cvt_pk_f16_f32 v57, v64, v65
	s_waitcnt vmcnt(2)
	v_cvt_pk_f16_f32 v2, v2, v3
	v_cvt_pk_f16_f32 v3, v4, v5
	v_cvt_pk_f16_f32 v4, v6, v7
	v_cvt_pk_f16_f32 v5, v8, v9
	v_mfma_f32_32x32x16_f16 v[90:105], v[34:37], v[222:225], 0
	v_cvt_pk_f16_f32 v6, v10, v11
	v_cvt_pk_f16_f32 v7, v12, v13
	v_cvt_pk_f16_f32 v8, v14, v15
	v_cvt_pk_f16_f32 v9, v16, v17
	v_mfma_f32_32x32x16_f16 v[106:121], v[34:37], v[238:241], 0
	v_cvt_pk_f16_f32 v18, v18, v19
	v_cvt_pk_f16_f32 v19, v20, v21
	v_cvt_pk_f16_f32 v20, v22, v23
	v_cvt_pk_f16_f32 v21, v24, v25
	v_mfma_f32_32x32x16_f16 v[90:105], v[38:41], v[226:229], v[90:105]
	v_cvt_pk_f16_f32 v22, v26, v27
	v_cvt_pk_f16_f32 v23, v28, v29
	v_cvt_pk_f16_f32 v24, v30, v31
	v_cvt_pk_f16_f32 v25, v32, v33
	v_mfma_f32_32x32x16_f16 v[106:121], v[38:41], v[242:245], v[106:121]
	s_waitcnt lgkmcnt(0)
	v_mul_f32_e32 v66, v199, v207
	v_mul_f32_e32 v68, v199, v206
	v_mul_f32_e32 v67, v199, v209
	v_mfma_f32_32x32x16_f16 v[90:105], v[50:53], v[230:233], v[90:105]
	v_mul_f32_e32 v69, v199, v208
	v_fma_f32 v66, v198, v206, -v66
	v_fma_f32 v68, v198, v207, v68
	v_fma_f32 v67, v198, v208, -v67
	v_mfma_f32_32x32x16_f16 v[106:121], v[50:53], v[246:249], v[106:121]
	v_fma_f32 v69, v198, v209, v69
	v_cvt_pk_f16_f32 v214, v66, v67
	v_cvt_pk_f16_f32 v216, v68, v69
	v_mul_f32_e32 v70, v201, v211
	v_mfma_f32_32x32x16_f16 v[90:105], v[54:57], v[234:237], v[90:105]
	v_mul_f32_e32 v72, v201, v210
	v_mul_f32_e32 v71, v201, v213
	v_mul_f32_e32 v73, v201, v212
	v_fma_f32 v70, v200, v210, -v70
	v_mfma_f32_32x32x16_f16 v[106:121], v[54:57], v[250:253], v[106:121]
	v_fma_f32 v72, v200, v211, v72
	v_fma_f32 v71, v200, v212, -v71
	v_fma_f32 v73, v200, v213, v73
	v_cvt_pk_f16_f32 v215, v70, v71
	v_cvt_pk_f16_f32 v217, v72, v73
	v_mfma_f32_32x32x16_f16 v[34:49], v[2:5], v[150:153], 0
	v_mul_f32_e32 v66, v203, v207
	v_mul_f32_e32 v68, v203, v206
	v_mul_f32_e32 v67, v203, v209
	v_mul_f32_e32 v69, v203, v208
	v_fma_f32 v66, v202, v206, -v66
	v_mfma_f32_32x32x16_f16 v[34:49], v[18:21], v[146:149], v[34:49]
	v_fma_f32 v68, v202, v207, v68
	v_fma_f32 v67, v202, v208, -v67
	v_fma_f32 v69, v202, v209, v69
	v_cvt_pk_f16_f32 v218, v66, v67
	v_cvt_pk_f16_f32 v220, v68, v69
	v_mfma_f32_32x32x16_f16 v[34:49], v[6:9], v[142:145], v[34:49]
	v_mul_f32_e32 v70, v205, v211
	v_mul_f32_e32 v72, v205, v210
	v_mul_f32_e32 v71, v205, v213
	v_mul_f32_e32 v73, v205, v212
	v_fma_f32 v70, v204, v210, -v70
	v_mfma_f32_32x32x16_f16 v[34:49], v[22:25], v[138:141], v[34:49]
	v_fma_f32 v72, v204, v211, v72
	v_fma_f32 v71, v204, v212, -v71
	v_fma_f32 v73, v204, v213, v73
	v_cvt_pk_f16_f32 v219, v70, v71
	v_cvt_pk_f16_f32 v221, v72, v73
	v_mfma_f32_32x32x16_f16 v[50:65], v[2:5], v[134:137], 0
	v_cvt_pk_f16_f32 v90, v90, v91
	v_cvt_pk_f16_f32 v91, v92, v93
	v_cvt_pk_f16_f32 v92, v94, v95
	v_cvt_pk_f16_f32 v93, v96, v97
	v_cvt_pk_f16_f32 v94, v98, v99
	v_mfma_f32_32x32x16_f16 v[50:65], v[18:21], v[126:129], v[50:65]
	v_cvt_pk_f16_f32 v95, v100, v101
	v_cvt_pk_f16_f32 v96, v102, v103
	v_cvt_pk_f16_f32 v97, v104, v105
	v_cvt_pk_f16_f32 v106, v106, v107
	v_cvt_pk_f16_f32 v107, v108, v109
	v_mfma_f32_32x32x16_f16 v[50:65], v[6:9], v[122:125], v[50:65]
	v_cvt_pk_f16_f32 v108, v110, v111
	v_cvt_pk_f16_f32 v109, v112, v113
	v_cvt_pk_f16_f32 v110, v114, v115
	v_cvt_pk_f16_f32 v111, v116, v117
	v_cvt_pk_f16_f32 v112, v118, v119
	v_mfma_f32_32x32x16_f16 v[50:65], v[22:25], v[130:133], v[50:65]
	v_cvt_pk_f16_f32 v113, v120, v121
	ds_write_b128 v173, v[90:93]
	ds_write_b128 v172, v[94:97]
	ds_write_b128 v173, v[106:109] offset:32768
	ds_write_b128 v172, v[110:113] offset:32768
	v_xor_b32_e32 v255, 24, v254
	ds_read2_b64 v[206:209], v255 offset0:0 offset1:16
	ds_read2_b64 v[210:213], v255 offset0:32 offset1:48
	v_mfma_f32_32x32x16_f16 v[2:17], v[190:193], v[214:217], 0
	v_mfma_f32_32x32x16_f16 v[18:33], v[194:197], v[218:221], 0
	v_cvt_pk_f16_f32 v34, v34, v35
	v_cvt_pk_f16_f32 v35, v36, v37
	v_cvt_pk_f16_f32 v36, v38, v39
	v_cvt_pk_f16_f32 v37, v40, v41
	v_cvt_pk_f16_f32 v38, v42, v43
	v_cvt_pk_f16_f32 v39, v44, v45
	v_cvt_pk_f16_f32 v40, v46, v47
	v_cvt_pk_f16_f32 v41, v48, v49
	v_cvt_pk_f16_f32 v50, v50, v51
	v_cvt_pk_f16_f32 v51, v52, v53
	v_cvt_pk_f16_f32 v52, v54, v55
	v_cvt_pk_f16_f32 v53, v56, v57
	v_cvt_pk_f16_f32 v54, v58, v59
	v_cvt_pk_f16_f32 v55, v60, v61
	v_cvt_pk_f16_f32 v56, v62, v63
	v_cvt_pk_f16_f32 v57, v64, v65
	v_mfma_f32_32x32x16_f16 v[90:105], v[34:37], v[222:225], 0
	v_cvt_pk_f16_f32 v2, v2, v3
	v_cvt_pk_f16_f32 v3, v4, v5
	v_cvt_pk_f16_f32 v4, v6, v7
	v_cvt_pk_f16_f32 v5, v8, v9
	v_mfma_f32_32x32x16_f16 v[106:121], v[34:37], v[238:241], 0
	v_cvt_pk_f16_f32 v6, v10, v11
	v_cvt_pk_f16_f32 v7, v12, v13
	v_cvt_pk_f16_f32 v8, v14, v15
	v_cvt_pk_f16_f32 v9, v16, v17
	v_cvt_pk_f16_f32 v18, v18, v19
	v_mfma_f32_32x32x16_f16 v[90:105], v[38:41], v[226:229], v[90:105]
	v_cvt_pk_f16_f32 v19, v20, v21
	v_cvt_pk_f16_f32 v20, v22, v23
	v_cvt_pk_f16_f32 v21, v24, v25
	v_cvt_pk_f16_f32 v22, v26, v27
	v_mfma_f32_32x32x16_f16 v[106:121], v[38:41], v[242:245], v[106:121]
	v_cvt_pk_f16_f32 v23, v28, v29
	v_cvt_pk_f16_f32 v24, v30, v31
	v_cvt_pk_f16_f32 v25, v32, v33
	s_waitcnt lgkmcnt(0)
	v_mul_f32_e32 v66, v199, v207
	v_mfma_f32_32x32x16_f16 v[90:105], v[50:53], v[230:233], v[90:105]
	v_mul_f32_e32 v68, v199, v206
	v_mul_f32_e32 v67, v199, v209
	v_mul_f32_e32 v69, v199, v208
	v_fma_f32 v66, v198, v206, -v66
	v_fma_f32 v68, v198, v207, v68
	v_mfma_f32_32x32x16_f16 v[106:121], v[50:53], v[246:249], v[106:121]
	v_fma_f32 v67, v198, v208, -v67
	v_fma_f32 v69, v198, v209, v69
	v_cvt_pk_f16_f32 v214, v66, v67
	v_cvt_pk_f16_f32 v216, v68, v69
	v_mfma_f32_32x32x16_f16 v[90:105], v[54:57], v[234:237], v[90:105]
	v_mul_f32_e32 v70, v201, v211
	v_mul_f32_e32 v72, v201, v210
	v_mul_f32_e32 v71, v201, v213
	v_mul_f32_e32 v73, v201, v212
	v_fma_f32 v70, v200, v210, -v70
	v_mfma_f32_32x32x16_f16 v[106:121], v[54:57], v[250:253], v[106:121]
	v_fma_f32 v72, v200, v211, v72
	v_fma_f32 v71, v200, v212, -v71
	v_fma_f32 v73, v200, v213, v73
	v_cvt_pk_f16_f32 v215, v70, v71
	v_cvt_pk_f16_f32 v217, v72, v73
	v_mfma_f32_32x32x16_f16 v[34:49], v[2:5], v[150:153], 0
	v_mul_f32_e32 v66, v203, v207
	v_mul_f32_e32 v68, v203, v206
	v_mul_f32_e32 v67, v203, v209
	v_mul_f32_e32 v69, v203, v208
	v_fma_f32 v66, v202, v206, -v66
	v_mfma_f32_32x32x16_f16 v[34:49], v[18:21], v[146:149], v[34:49]
	v_fma_f32 v68, v202, v207, v68
	v_fma_f32 v67, v202, v208, -v67
	v_fma_f32 v69, v202, v209, v69
	v_cvt_pk_f16_f32 v218, v66, v67
	v_cvt_pk_f16_f32 v220, v68, v69
	v_mfma_f32_32x32x16_f16 v[34:49], v[6:9], v[142:145], v[34:49]
	v_mul_f32_e32 v70, v205, v211
	v_mul_f32_e32 v72, v205, v210
	v_mul_f32_e32 v71, v205, v213
	v_mul_f32_e32 v73, v205, v212
	v_fma_f32 v70, v204, v210, -v70
	v_mfma_f32_32x32x16_f16 v[34:49], v[22:25], v[138:141], v[34:49]
	v_fma_f32 v72, v204, v211, v72
	v_fma_f32 v71, v204, v212, -v71
	v_fma_f32 v73, v204, v213, v73
	v_cvt_pk_f16_f32 v219, v70, v71
	v_cvt_pk_f16_f32 v221, v72, v73
	v_cvt_pk_f16_f32 v90, v90, v91
	v_mfma_f32_32x32x16_f16 v[50:65], v[2:5], v[134:137], 0
	v_cvt_pk_f16_f32 v91, v92, v93
	v_cvt_pk_f16_f32 v92, v94, v95
	v_cvt_pk_f16_f32 v93, v96, v97
	v_cvt_pk_f16_f32 v94, v98, v99
	v_cvt_pk_f16_f32 v95, v100, v101
	v_mfma_f32_32x32x16_f16 v[50:65], v[18:21], v[126:129], v[50:65]
	v_cvt_pk_f16_f32 v96, v102, v103
	v_cvt_pk_f16_f32 v97, v104, v105
	v_cvt_pk_f16_f32 v106, v106, v107
	v_cvt_pk_f16_f32 v107, v108, v109
	v_cvt_pk_f16_f32 v108, v110, v111
	v_mfma_f32_32x32x16_f16 v[50:65], v[6:9], v[122:125], v[50:65]
	v_cvt_pk_f16_f32 v109, v112, v113
	v_cvt_pk_f16_f32 v110, v114, v115
	v_cvt_pk_f16_f32 v111, v116, v117
	v_cvt_pk_f16_f32 v112, v118, v119
	v_cvt_pk_f16_f32 v113, v120, v121
	v_mfma_f32_32x32x16_f16 v[50:65], v[22:25], v[130:133], v[50:65]
	v_xor_b32_e32 v74, 0x8a0, v173
	v_xor_b32_e32 v75, 0x8a0, v172
	ds_write_b128 v74, v[90:93]
	ds_write_b128 v75, v[94:97]
	ds_write_b128 v74, v[106:109] offset:32768
	ds_write_b128 v75, v[110:113] offset:32768
	s_nop 0
	v_mfma_f32_32x32x16_f16 v[2:17], v[190:193], v[214:217], 0
	v_mfma_f32_32x32x16_f16 v[18:33], v[194:197], v[218:221], 0
	v_cvt_pk_f16_f32 v34, v34, v35
	v_cvt_pk_f16_f32 v35, v36, v37
	v_cvt_pk_f16_f32 v36, v38, v39
	v_cvt_pk_f16_f32 v37, v40, v41
	v_cvt_pk_f16_f32 v38, v42, v43
	v_cvt_pk_f16_f32 v39, v44, v45
	v_cvt_pk_f16_f32 v40, v46, v47
	v_cvt_pk_f16_f32 v41, v48, v49
	v_cvt_pk_f16_f32 v50, v50, v51
	v_cvt_pk_f16_f32 v51, v52, v53
	v_cvt_pk_f16_f32 v52, v54, v55
	v_cvt_pk_f16_f32 v53, v56, v57
	v_cvt_pk_f16_f32 v54, v58, v59
	v_cvt_pk_f16_f32 v55, v60, v61
	v_cvt_pk_f16_f32 v56, v62, v63
	v_cvt_pk_f16_f32 v57, v64, v65
	v_mfma_f32_32x32x16_f16 v[90:105], v[34:37], v[222:225], 0
	v_cvt_pk_f16_f32 v2, v2, v3
	v_cvt_pk_f16_f32 v3, v4, v5
	v_mfma_f32_32x32x16_f16 v[106:121], v[34:37], v[238:241], 0
	v_cvt_pk_f16_f32 v4, v6, v7
	v_cvt_pk_f16_f32 v5, v8, v9
	v_mfma_f32_32x32x16_f16 v[90:105], v[38:41], v[226:229], v[90:105]
	v_cvt_pk_f16_f32 v6, v10, v11
	v_cvt_pk_f16_f32 v7, v12, v13
	v_mfma_f32_32x32x16_f16 v[106:121], v[38:41], v[242:245], v[106:121]
	v_cvt_pk_f16_f32 v8, v14, v15
	v_cvt_pk_f16_f32 v9, v16, v17
	v_mfma_f32_32x32x16_f16 v[90:105], v[50:53], v[230:233], v[90:105]
	v_cvt_pk_f16_f32 v18, v18, v19
	v_cvt_pk_f16_f32 v19, v20, v21
	v_mfma_f32_32x32x16_f16 v[106:121], v[50:53], v[246:249], v[106:121]
	v_cvt_pk_f16_f32 v20, v22, v23
	v_cvt_pk_f16_f32 v21, v24, v25
	v_mfma_f32_32x32x16_f16 v[90:105], v[54:57], v[234:237], v[90:105]
	v_cvt_pk_f16_f32 v22, v26, v27
	v_cvt_pk_f16_f32 v23, v28, v29
	v_mfma_f32_32x32x16_f16 v[106:121], v[54:57], v[250:253], v[106:121]
	v_cvt_pk_f16_f32 v24, v30, v31
	v_cvt_pk_f16_f32 v25, v32, v33
	v_mfma_f32_32x32x16_f16 v[34:49], v[2:5], v[150:153], 0
	v_mfma_f32_32x32x16_f16 v[34:49], v[18:21], v[146:149], v[34:49]
	v_mfma_f32_32x32x16_f16 v[34:49], v[6:9], v[142:145], v[34:49]
	v_mfma_f32_32x32x16_f16 v[34:49], v[22:25], v[138:141], v[34:49]
	v_mfma_f32_32x32x16_f16 v[50:65], v[2:5], v[134:137], 0
	s_nop 5
	v_cvt_pk_f16_f32 v90, v90, v91
	v_cvt_pk_f16_f32 v91, v92, v93
	v_cvt_pk_f16_f32 v92, v94, v95
	v_cvt_pk_f16_f32 v93, v96, v97
	v_mfma_f32_32x32x16_f16 v[50:65], v[18:21], v[126:129], v[50:65]
	v_cvt_pk_f16_f32 v94, v98, v99
	v_cvt_pk_f16_f32 v95, v100, v101
	v_cvt_pk_f16_f32 v96, v102, v103
	v_cvt_pk_f16_f32 v97, v104, v105
	v_cvt_pk_f16_f32 v106, v106, v107
	v_cvt_pk_f16_f32 v107, v108, v109
	v_mfma_f32_32x32x16_f16 v[50:65], v[6:9], v[122:125], v[50:65]
	v_cvt_pk_f16_f32 v108, v110, v111
	v_cvt_pk_f16_f32 v109, v112, v113
	v_cvt_pk_f16_f32 v110, v114, v115
	v_cvt_pk_f16_f32 v111, v116, v117
	v_cvt_pk_f16_f32 v112, v118, v119
	v_cvt_pk_f16_f32 v113, v120, v121
	v_mfma_f32_32x32x16_f16 v[50:65], v[22:25], v[130:133], v[50:65]
	v_xor_b32_e32 v74, 0x1040, v173
	v_xor_b32_e32 v75, 0x1040, v172
	ds_write_b128 v74, v[90:93]
	ds_write_b128 v75, v[94:97]
	ds_write_b128 v74, v[106:109] offset:32768
	ds_write_b128 v75, v[110:113] offset:32768
	s_nop 11
	v_cvt_pk_f16_f32 v34, v34, v35
	v_cvt_pk_f16_f32 v35, v36, v37
	v_cvt_pk_f16_f32 v36, v38, v39
	v_cvt_pk_f16_f32 v37, v40, v41
	v_cvt_pk_f16_f32 v38, v42, v43
	v_cvt_pk_f16_f32 v39, v44, v45
	v_cvt_pk_f16_f32 v40, v46, v47
	v_cvt_pk_f16_f32 v41, v48, v49
	v_cvt_pk_f16_f32 v50, v50, v51
	v_cvt_pk_f16_f32 v51, v52, v53
	v_cvt_pk_f16_f32 v52, v54, v55
	v_cvt_pk_f16_f32 v53, v56, v57
	v_cvt_pk_f16_f32 v54, v58, v59
	v_cvt_pk_f16_f32 v55, v60, v61
	v_cvt_pk_f16_f32 v56, v62, v63
	v_cvt_pk_f16_f32 v57, v64, v65
	v_mfma_f32_32x32x16_f16 v[90:105], v[34:37], v[222:225], 0
	v_mfma_f32_32x32x16_f16 v[106:121], v[34:37], v[238:241], 0
	v_mfma_f32_32x32x16_f16 v[90:105], v[38:41], v[226:229], v[90:105]
	v_mfma_f32_32x32x16_f16 v[106:121], v[38:41], v[242:245], v[106:121]
	v_mfma_f32_32x32x16_f16 v[90:105], v[50:53], v[230:233], v[90:105]
	v_mfma_f32_32x32x16_f16 v[106:121], v[50:53], v[246:249], v[106:121]
	v_mfma_f32_32x32x16_f16 v[90:105], v[54:57], v[234:237], v[90:105]
	v_mfma_f32_32x32x16_f16 v[106:121], v[54:57], v[250:253], v[106:121]
	v_and_b32_e32 v134, 1, v156
	v_bitop3_b32 v132, v171, s40, v170 bitop3:0x36
	v_bitop3_b32 v131, s41, v154, v160 bitop3:0x36
	v_bitop3_b32 v135, v171, s42, v170 bitop3:0x36
	v_xor_b32_e32 v133, s43, v154
	v_and_b32_e32 v130, 4, v156
	s_lshl_b32 s2, s27, 3
	s_lshl_b32 s3, s5, 2
	s_or_b32 s2, s3, s2
	s_ashr_i32 s3, s2, 31
	s_lshl_b64 s[2:3], s[2:3], 13
	s_add_u32 s2, s20, s2
	s_addc_u32 s3, s21, s3
	v_lshlrev_b32_e32 v154, 1, v169
	v_lshl_add_u64 v[2:3], s[2:3], 0, v[154:155]
	v_add_co_u32_e32 v2, vcc, s23, v2
	s_nop 1
	v_addc_co_u32_e32 v3, vcc, 0, v3, vcc
	v_cvt_pk_f16_f32 v90, v90, v91
	v_cvt_pk_f16_f32 v91, v92, v93
	v_cvt_pk_f16_f32 v92, v94, v95
	v_cvt_pk_f16_f32 v93, v96, v97
	v_cvt_pk_f16_f32 v94, v98, v99
	v_cvt_pk_f16_f32 v95, v100, v101
	v_cvt_pk_f16_f32 v96, v102, v103
	v_cvt_pk_f16_f32 v97, v104, v105
	v_cvt_pk_f16_f32 v106, v106, v107
	v_cvt_pk_f16_f32 v107, v108, v109
	v_cvt_pk_f16_f32 v108, v110, v111
	v_cvt_pk_f16_f32 v109, v112, v113
	v_cvt_pk_f16_f32 v110, v114, v115
	v_cvt_pk_f16_f32 v111, v116, v117
	v_cvt_pk_f16_f32 v112, v118, v119
	v_cvt_pk_f16_f32 v113, v120, v121
	v_xor_b32_e32 v74, 0x18e0, v173
	v_xor_b32_e32 v75, 0x18e0, v172
	ds_write_b128 v74, v[90:93]
	ds_write_b128 v75, v[94:97]
	ds_write_b128 v74, v[106:109] offset:32768
	ds_write_b128 v75, v[110:113] offset:32768
	s_setprio 0
	s_waitcnt lgkmcnt(0)
	s_barrier
	global_load_dwordx4 v[62:65], v154, s[2:3]
	global_load_dwordx4 v[46:49], v154, s[2:3] offset:1024
	global_load_dwordx4 v[42:45], v154, s[2:3] offset:2048
	global_load_dwordx4 v[38:41], v154, s[2:3] offset:3072
	global_load_dwordx4 v[54:57], v[2:3], off offset:1024
	global_load_dwordx4 v[50:53], v[2:3], off offset:2048
	v_lshl_add_u64 v[4:5], s[12:13], 0, v[154:155]
	global_load_dwordx4 v[126:129], v154, s[12:13]
	global_load_dwordx4 v[122:125], v154, s[12:13] offset:1024
	global_load_dwordx4 v[118:121], v154, s[12:13] offset:2048
	global_load_dwordx4 v[114:117], v154, s[12:13] offset:3072
	global_load_dwordx4 v[34:37], v168, s[2:3]
	global_load_dwordx4 v[110:113], v168, s[12:13]
	v_add_co_u32_e32 v4, vcc, s23, v4
	s_nop 1
	v_addc_co_u32_e32 v5, vcc, 0, v5, vcc
	global_load_dwordx4 v[58:61], v[2:3], off offset:3072
	global_load_dwordx4 v[106:109], v[4:5], off offset:1024
	global_load_dwordx4 v[94:97], v[4:5], off offset:2048
	global_load_dwordx4 v[90:93], v[4:5], off offset:3072
	v_bfrev_b32_e32 v3, v156
	v_lshlrev_b32_e32 v7, 5, v167
	v_lshlrev_b32_e32 v6, 9, v167
	v_and_b32_e32 v7, 0x200, v7
	v_lshlrev_b32_e32 v8, 8, v167
	v_lshrrev_b32_e32 v3, 27, v3
	v_lshrrev_b32_e32 v2, 2, v167
	v_lshrrev_b32_e32 v4, 4, v156
	v_xor_b32_e32 v5, v169, v156
	v_and_b32_e32 v6, 0x5800, v6
	v_and_b32_e32 v3, 8, v3
	v_and_or_b32 v7, v8, s24, v7
	v_lshrrev_b32_e32 v5, 1, v5
	v_xor_b32_e32 v4, v2, v4
	v_or3_b32 v3, v7, v6, v3
	v_bitop3_b32 v7, v2, v182, 1 bitop3:0x6c
	v_lshlrev_b32_e32 v2, 1, v167
	v_and_b32_e32 v5, 4, v5
	v_lshlrev_b32_e32 v4, 3, v4
	v_lshrrev_b32_e32 v6, 1, v167
	v_and_b32_e32 v2, 2, v2
	v_and_or_b32 v9, v169, 8, v2
	v_and_b32_e32 v2, 8, v4
	v_and_or_b32 v4, v6, 2, v5
	v_or3_b32 v2, v4, v2, v134
	v_lshlrev_b32_e32 v2, 4, v2
	v_bitop3_b32 v146, v3, s28, v2 bitop3:0x36
	v_xor_b32_e32 v8, v6, v182
	v_xor_b32_e32 v147, 0x2010, v146
	v_lshlrev_b32_e32 v8, 2, v8
	v_and_b32_e32 v8, 4, v8
	v_or3_b32 v6, v9, v7, v8
	v_lshlrev_b32_e32 v7, 11, v167
	v_and_b32_e32 v8, 0x7800, v7
	v_lshlrev_b32_e32 v6, 4, v6
	v_or3_b32 v22, v6, v8, v170
	v_and_b32_e32 v23, 0x8000, v7
	v_xor_b32_e32 v150, 16, v146
	v_xad_u32 v70, v22, s28, v23
	v_xor_b32_e32 v151, 0x2000, v146
	ds_read_b64_tr_b16 v[18:19], v146
	ds_read_b64_tr_b16 v[20:21], v147
	ds_read_b64_tr_b16 v[22:23], v146 offset:32768
	ds_read_b64_tr_b16 v[24:25], v147 offset:32768
	ds_read_b64_tr_b16 v[26:27], v150
	ds_read_b64_tr_b16 v[28:29], v151
	ds_read_b64_tr_b16 v[30:31], v150 offset:32768
	ds_read_b64_tr_b16 v[32:33], v151 offset:32768
	v_xor_b32_e32 v148, 32, v146
	v_xor_b32_e32 v149, 0x2030, v146
	v_xor_b32_e32 v144, 48, v146
	v_xor_b32_e32 v145, 0x2020, v146
	v_xor_b32_e32 v142, 64, v146
	v_xor_b32_e32 v143, 0x2050, v146
	v_xor_b32_e32 v140, 0x50, v146
	v_xor_b32_e32 v141, 0x2040, v146
	v_xor_b32_e32 v138, 0x60, v146
	v_xor_b32_e32 v139, 0x2070, v146
	v_xor_b32_e32 v136, 0x70, v146
	v_xor_b32_e32 v137, 0x2060, v146
	v_xor_b32_e32 v71, 0x60, v70
	s_lshl_b64 s[0:1], s[0:1], 13
	s_add_u32 s0, s8, s0
	s_addc_u32 s1, s9, s1
	s_waitcnt vmcnt(17) lgkmcnt(4)
	v_mfma_f32_32x32x16_f16 v[2:17], v[18:21], v[86:89], 0
	s_waitcnt vmcnt(16)
	v_mfma_f32_32x32x16_f16 v[2:17], v[22:25], v[82:85], v[2:17]
	ds_read_b64_tr_b16 v[206:207], v148
	ds_read_b64_tr_b16 v[208:209], v149
	ds_read_b64_tr_b16 v[210:211], v148 offset:32768
	ds_read_b64_tr_b16 v[212:213], v149 offset:32768
	s_waitcnt lgkmcnt(4)
	v_mfma_f32_32x32x16_f16 v[190:205], v[26:29], v[86:89], 0
	v_mfma_f32_32x32x16_f16 v[190:205], v[30:33], v[82:85], v[190:205]
	s_nop 4
	v_cvt_pk_f16_f32 v2, v2, v3
	v_cvt_pk_f16_f32 v3, v4, v5
	v_cvt_pk_f16_f32 v4, v6, v7
	v_cvt_pk_f16_f32 v5, v8, v9
	v_cvt_pk_f16_f32 v6, v10, v11
	v_cvt_pk_f16_f32 v7, v12, v13
	v_cvt_pk_f16_f32 v8, v14, v15
	v_cvt_pk_f16_f32 v9, v16, v17
	v_xor_b32_e32 v73, 0x280, v70
	ds_write_b128 v70, v[2:5]
	ds_write_b128 v73, v[6:9]
	ds_read_b64_tr_b16 v[18:19], v144
	ds_read_b64_tr_b16 v[20:21], v145
	ds_read_b64_tr_b16 v[22:23], v144 offset:32768
	ds_read_b64_tr_b16 v[24:25], v145 offset:32768
	s_waitcnt lgkmcnt(6)
	v_mfma_f32_32x32x16_f16 v[2:17], v[206:209], v[86:89], 0
	v_mfma_f32_32x32x16_f16 v[2:17], v[210:213], v[82:85], v[2:17]
	v_cvt_pk_f16_f32 v190, v190, v191
	v_cvt_pk_f16_f32 v191, v192, v193
	v_cvt_pk_f16_f32 v192, v194, v195
	v_cvt_pk_f16_f32 v193, v196, v197
	v_cvt_pk_f16_f32 v194, v198, v199
	v_cvt_pk_f16_f32 v195, v200, v201
	v_cvt_pk_f16_f32 v196, v202, v203
	v_cvt_pk_f16_f32 v197, v204, v205
	v_xor_b32_e32 v72, 16, v70
	v_xor_b32_e32 v73, 0x290, v70
	ds_write_b128 v72, v[190:193]
	ds_write_b128 v73, v[194:197]
	ds_read_b64_tr_b16 v[26:27], v142
	ds_read_b64_tr_b16 v[28:29], v143
	ds_read_b64_tr_b16 v[30:31], v142 offset:32768
	ds_read_b64_tr_b16 v[32:33], v143 offset:32768
	s_waitcnt lgkmcnt(6)
	v_mfma_f32_32x32x16_f16 v[190:205], v[18:21], v[86:89], 0
	v_mfma_f32_32x32x16_f16 v[190:205], v[22:25], v[82:85], v[190:205]
	v_cvt_pk_f16_f32 v2, v2, v3
	v_cvt_pk_f16_f32 v3, v4, v5
	v_cvt_pk_f16_f32 v4, v6, v7
	v_cvt_pk_f16_f32 v5, v8, v9
	v_cvt_pk_f16_f32 v6, v10, v11
	v_cvt_pk_f16_f32 v7, v12, v13
	v_cvt_pk_f16_f32 v8, v14, v15
	v_cvt_pk_f16_f32 v9, v16, v17
	v_xor_b32_e32 v72, 32, v70
	v_xor_b32_e32 v73, 0x2a0, v70
	ds_write_b128 v72, v[2:5]
	ds_write_b128 v73, v[6:9]
	ds_read_b64_tr_b16 v[206:207], v140
	ds_read_b64_tr_b16 v[208:209], v141
	ds_read_b64_tr_b16 v[210:211], v140 offset:32768
	ds_read_b64_tr_b16 v[212:213], v141 offset:32768
	s_waitcnt lgkmcnt(6)
	v_mfma_f32_32x32x16_f16 v[2:17], v[26:29], v[86:89], 0
	v_mfma_f32_32x32x16_f16 v[2:17], v[30:33], v[82:85], v[2:17]
	v_cvt_pk_f16_f32 v190, v190, v191
	v_cvt_pk_f16_f32 v191, v192, v193
	v_cvt_pk_f16_f32 v192, v194, v195
	v_cvt_pk_f16_f32 v193, v196, v197
	v_cvt_pk_f16_f32 v194, v198, v199
	v_cvt_pk_f16_f32 v195, v200, v201
	v_cvt_pk_f16_f32 v196, v202, v203
	v_cvt_pk_f16_f32 v197, v204, v205
	v_xor_b32_e32 v72, 48, v70
	v_xor_b32_e32 v73, 0x2b0, v70
	ds_write_b128 v72, v[190:193]
	ds_write_b128 v73, v[194:197]
	ds_read_b64_tr_b16 v[18:19], v138
	ds_read_b64_tr_b16 v[20:21], v139
	ds_read_b64_tr_b16 v[22:23], v138 offset:32768
	ds_read_b64_tr_b16 v[24:25], v139 offset:32768
	s_waitcnt lgkmcnt(6)
	v_mfma_f32_32x32x16_f16 v[190:205], v[206:209], v[86:89], 0
	v_mfma_f32_32x32x16_f16 v[190:205], v[210:213], v[82:85], v[190:205]
	v_cvt_pk_f16_f32 v2, v2, v3
	v_cvt_pk_f16_f32 v3, v4, v5
	v_cvt_pk_f16_f32 v4, v6, v7
	v_cvt_pk_f16_f32 v5, v8, v9
	v_cvt_pk_f16_f32 v6, v10, v11
	v_cvt_pk_f16_f32 v7, v12, v13
	v_cvt_pk_f16_f32 v8, v14, v15
	v_cvt_pk_f16_f32 v9, v16, v17
	v_xor_b32_e32 v72, 64, v70
	v_xor_b32_e32 v73, 0x2c0, v70
	ds_write_b128 v72, v[2:5]
	ds_write_b128 v73, v[6:9]
	ds_read_b64_tr_b16 v[26:27], v136
	ds_read_b64_tr_b16 v[28:29], v137
	ds_read_b64_tr_b16 v[30:31], v136 offset:32768
	ds_read_b64_tr_b16 v[32:33], v137 offset:32768
	s_waitcnt lgkmcnt(6)
	v_mfma_f32_32x32x16_f16 v[2:17], v[18:21], v[86:89], 0
	v_mfma_f32_32x32x16_f16 v[2:17], v[22:25], v[82:85], v[2:17]
	v_cvt_pk_f16_f32 v190, v190, v191
	v_cvt_pk_f16_f32 v191, v192, v193
	v_cvt_pk_f16_f32 v192, v194, v195
	v_cvt_pk_f16_f32 v193, v196, v197
	v_cvt_pk_f16_f32 v194, v198, v199
	v_cvt_pk_f16_f32 v195, v200, v201
	v_cvt_pk_f16_f32 v196, v202, v203
	v_cvt_pk_f16_f32 v197, v204, v205
	v_xor_b32_e32 v72, 0x50, v70
	v_xor_b32_e32 v73, 0x2d0, v70
	ds_write_b128 v72, v[190:193]
	ds_write_b128 v73, v[194:197]
	s_waitcnt lgkmcnt(2)
	v_mfma_f32_32x32x16_f16 v[190:205], v[26:29], v[86:89], 0
	v_mfma_f32_32x32x16_f16 v[190:205], v[30:33], v[82:85], v[190:205]
	v_cvt_pk_f16_f32 v2, v2, v3
	v_cvt_pk_f16_f32 v3, v4, v5
	v_cvt_pk_f16_f32 v4, v6, v7
	v_cvt_pk_f16_f32 v5, v8, v9
	v_cvt_pk_f16_f32 v6, v10, v11
	v_cvt_pk_f16_f32 v7, v12, v13
	v_cvt_pk_f16_f32 v8, v14, v15
	v_cvt_pk_f16_f32 v9, v16, v17
	v_xor_b32_e32 v72, 0x60, v70
	v_xor_b32_e32 v73, 0x2e0, v70
	ds_write_b128 v72, v[2:5]
	ds_write_b128 v73, v[6:9]
	v_cvt_pk_f16_f32 v190, v190, v191
	v_cvt_pk_f16_f32 v191, v192, v193
	v_cvt_pk_f16_f32 v192, v194, v195
	v_cvt_pk_f16_f32 v193, v196, v197
	v_cvt_pk_f16_f32 v194, v198, v199
	v_cvt_pk_f16_f32 v195, v200, v201
	v_cvt_pk_f16_f32 v196, v202, v203
	v_cvt_pk_f16_f32 v197, v204, v205
	v_xor_b32_e32 v72, 0x70, v70
	v_xor_b32_e32 v73, 0x2f0, v70
	ds_write_b128 v72, v[190:193]
	ds_write_b128 v73, v[194:197]
	v_lshl_add_u64 v[2:3], s[0:1], 0, v[154:155]
	v_lshl_add_u64 v[4:5], v[2:3], 0, s[18:19]
	v_add_co_u32_e32 v2, vcc, s25, v2
	s_waitcnt lgkmcnt(0)
	s_nop 0
	v_addc_co_u32_e32 v3, vcc, 0, v3, vcc
	s_barrier
	s_nop 0
	s_nop 0
	global_load_dwordx4 v[102:105], v[2:3], off
	global_load_dwordx4 v[98:101], v[4:5], off offset:1024
	s_setprio 1
	s_add_u32 s0, s2, 0x2000
	s_addc_u32 s1, s3, 0
	v_lshl_add_u64 v[2:3], s[0:1], 0, v[154:155]
	v_add_co_u32_e32 v2, vcc, s23, v2
	global_load_dwordx4 v[66:69], v154, s[0:1]
	global_load_dwordx4 v[70:73], v154, s[0:1] offset:1024
	global_load_dwordx4 v[74:77], v154, s[0:1] offset:2048
	global_load_dwordx4 v[78:81], v154, s[0:1] offset:3072
	v_addc_co_u32_e32 v3, vcc, 0, v3, vcc
	global_load_dwordx4 v[82:85], v168, s[0:1]
	global_load_dwordx4 v[86:89], v[2:3], off offset:1024
	global_load_dwordx4 v[182:185], v[2:3], off offset:2048
	global_load_dwordx4 v[186:189], v[2:3], off offset:3072
	ds_read_b128 v[18:21], v179
	ds_read_b128 v[22:25], v179 offset:32768
	ds_read_b128 v[26:29], v178
	ds_read_b128 v[30:33], v178 offset:32768
	s_add_u32 s0, s2, 0x6000
	s_addc_u32 s1, s3, 0
	s_waitcnt vmcnt(25) lgkmcnt(3)
	v_mfma_f32_32x32x16_f16 v[2:17], v[18:21], v[62:65], 0
	s_add_u32 s2, s2, 0x4000
	s_addc_u32 s3, s3, 0
	s_or_b32 s27, s26, 0x8a0
	s_or_b32 s26, s26, 0xa20
	s_waitcnt vmcnt(24) lgkmcnt(1)
	v_mfma_f32_32x32x16_f16 v[2:17], v[26:29], v[46:49], v[2:17]
	s_waitcnt vmcnt(23)
	v_mfma_f32_32x32x16_f16 v[2:17], v[22:25], v[42:45], v[2:17]
	s_waitcnt vmcnt(22) lgkmcnt(0)
	v_mfma_f32_32x32x16_f16 v[2:17], v[30:33], v[38:41], v[2:17]
	s_waitcnt vmcnt(15)
	v_mfma_f32_32x32x16_f16 v[34:49], v[18:21], v[34:37], 0
	s_nop 9
	v_cvt_pk_f16_f32 v9, v8, v9
	v_cvt_pk_f16_f32 v8, v6, v7
	v_cvt_pk_f16_f32 v7, v4, v5
	v_cvt_pk_f16_f32 v6, v2, v3
	v_cvt_pk_f16_f32 v5, v16, v17
	v_cvt_pk_f16_f32 v4, v14, v15
	v_cvt_pk_f16_f32 v3, v12, v13
	v_mfma_f32_32x32x16_f16 v[34:49], v[26:29], v[54:57], v[34:49]
	v_cvt_pk_f16_f32 v2, v10, v11
	v_mfma_f32_32x32x16_f16 v[34:49], v[22:25], v[50:53], v[34:49]
	s_waitcnt vmcnt(13)
	v_mfma_f32_32x32x16_f16 v[34:49], v[30:33], v[58:61], v[34:49]
	v_mfma_f32_32x32x16_f16 v[18:33], v[6:9], v[126:129], 0
	s_nop 10
	v_cvt_pk_f16_f32 v13, v40, v41
	v_cvt_pk_f16_f32 v12, v38, v39
	v_cvt_pk_f16_f32 v11, v36, v37
	v_cvt_pk_f16_f32 v10, v34, v35
	v_cvt_pk_f16_f32 v17, v48, v49
	v_cvt_pk_f16_f32 v16, v46, v47
	v_cvt_pk_f16_f32 v15, v44, v45
	v_mfma_f32_32x32x16_f16 v[50:65], v[6:9], v[110:113], 0
	v_bitop3_b32 v6, v171, s27, v170 bitop3:0x36
	v_cvt_pk_f16_f32 v14, v42, v43
	v_mfma_f32_32x32x16_f16 v[18:33], v[2:5], v[122:125], v[18:33]
	s_waitcnt vmcnt(12)
	v_mfma_f32_32x32x16_f16 v[50:65], v[2:5], v[106:109], v[50:65]
	ds_read_b128 v[2:5], v6
	ds_read_b128 v[6:9], v6 offset:32768
	v_mfma_f32_32x32x16_f16 v[18:33], v[10:13], v[118:121], v[18:33]
	s_waitcnt vmcnt(11)
	v_mfma_f32_32x32x16_f16 v[50:65], v[10:13], v[94:97], v[50:65]
	s_waitcnt vmcnt(7) lgkmcnt(1)
	v_mfma_f32_32x32x16_f16 v[34:49], v[2:5], v[66:69], 0
	v_mfma_f32_32x32x16_f16 v[18:33], v[14:17], v[114:117], v[18:33]
	v_mfma_f32_32x32x16_f16 v[50:65], v[14:17], v[90:93], v[50:65]
	v_bitop3_b32 v14, v171, s26, v170 bitop3:0x36
	ds_read_b128 v[10:13], v14
	ds_read_b128 v[14:17], v14 offset:32768
	s_nop 7
	v_cvt_pk_f16_f32 v25, v24, v25
	v_cvt_pk_f16_f32 v24, v22, v23
	v_cvt_pk_f16_f32 v23, v20, v21
	v_cvt_pk_f16_f32 v22, v18, v19
	v_cvt_pk_f16_f32 v21, v32, v33
	s_waitcnt vmcnt(6) lgkmcnt(1)
	v_mfma_f32_32x32x16_f16 v[34:49], v[10:13], v[70:73], v[34:49]
	v_cvt_pk_f16_f32 v20, v30, v31
	v_cvt_pk_f16_f32 v19, v28, v29
	v_cvt_pk_f16_f32 v18, v26, v27
	ds_write_b128 v173, v[22:25]
	ds_write_b128 v172, v[18:21]
	v_cvt_pk_f16_f32 v21, v56, v57
	v_cvt_pk_f16_f32 v20, v54, v55
	s_waitcnt vmcnt(5)
	v_mfma_f32_32x32x16_f16 v[34:49], v[6:9], v[74:77], v[34:49]
	v_cvt_pk_f16_f32 v19, v52, v53
	v_cvt_pk_f16_f32 v18, v50, v51
	ds_write_b128 v173, v[18:21] offset:32768
	v_cvt_pk_f16_f32 v21, v64, v65
	v_cvt_pk_f16_f32 v20, v62, v63
	v_cvt_pk_f16_f32 v19, v60, v61
	v_cvt_pk_f16_f32 v18, v58, v59
	s_waitcnt vmcnt(4) lgkmcnt(3)
	v_mfma_f32_32x32x16_f16 v[34:49], v[14:17], v[78:81], v[34:49]
	ds_write_b128 v172, v[18:21] offset:32768
	s_waitcnt vmcnt(3)
	v_mfma_f32_32x32x16_f16 v[66:81], v[2:5], v[82:85], 0
	s_nop 8
	v_cvt_pk_f16_f32 v41, v40, v41
	v_cvt_pk_f16_f32 v40, v38, v39
	v_cvt_pk_f16_f32 v39, v36, v37
	v_cvt_pk_f16_f32 v38, v34, v35
	v_cvt_pk_f16_f32 v85, v48, v49
	v_cvt_pk_f16_f32 v84, v46, v47
	v_cvt_pk_f16_f32 v83, v44, v45
	s_waitcnt vmcnt(2)
	v_mfma_f32_32x32x16_f16 v[66:81], v[10:13], v[86:89], v[66:81]
	v_cvt_pk_f16_f32 v82, v42, v43
	s_waitcnt vmcnt(1)
	v_mfma_f32_32x32x16_f16 v[66:81], v[6:9], v[182:185], v[66:81]
	s_waitcnt vmcnt(0)
	v_mfma_f32_32x32x16_f16 v[66:81], v[14:17], v[186:189], v[66:81]
	v_mfma_f32_32x32x16_f16 v[2:17], v[38:41], v[126:129], 0
	s_nop 10
	v_cvt_pk_f16_f32 v73, v72, v73
	v_cvt_pk_f16_f32 v72, v70, v71
	v_cvt_pk_f16_f32 v70, v66, v67
	v_cvt_pk_f16_f32 v67, v76, v77
	v_cvt_pk_f16_f32 v66, v74, v75
	global_load_dwordx4 v[74:77], v154, s[2:3]
	v_cvt_pk_f16_f32 v71, v68, v69
	v_cvt_pk_f16_f32 v69, v80, v81
	v_cvt_pk_f16_f32 v68, v78, v79
	global_load_dwordx4 v[78:81], v154, s[2:3] offset:1024
	ds_read_b128 v[18:21], v180
	ds_read_b128 v[22:25], v176
	ds_read_b128 v[26:29], v180 offset:32768
	global_load_dwordx4 v[30:33], v154, s[2:3] offset:2048
	v_mfma_f32_32x32x16_f16 v[34:49], v[38:41], v[110:113], 0
	v_mfma_f32_32x32x16_f16 v[2:17], v[82:85], v[122:125], v[2:17]
	v_mfma_f32_32x32x16_f16 v[34:49], v[82:85], v[106:109], v[34:49]
	ds_read_b128 v[82:85], v176 offset:32768
	s_waitcnt vmcnt(2) lgkmcnt(3)
	v_mfma_f32_32x32x16_f16 v[50:65], v[18:21], v[74:77], 0
	v_mfma_f32_32x32x16_f16 v[2:17], v[70:73], v[118:121], v[2:17]
	v_mfma_f32_32x32x16_f16 v[34:49], v[70:73], v[94:97], v[34:49]
	v_lshl_add_u64 v[70:71], s[2:3], 0, v[154:155]
	v_add_co_u32_e32 v152, vcc, s23, v70
	s_nop 1
	v_addc_co_u32_e32 v153, vcc, 0, v71, vcc
	s_waitcnt vmcnt(1) lgkmcnt(2)
	v_mfma_f32_32x32x16_f16 v[50:65], v[22:25], v[78:81], v[50:65]
	v_mfma_f32_32x32x16_f16 v[2:17], v[66:69], v[114:117], v[2:17]
	v_mfma_f32_32x32x16_f16 v[34:49], v[66:69], v[90:93], v[34:49]
	global_load_dwordx4 v[66:69], v154, s[2:3] offset:3072
	s_nop 9
	v_cvt_pk_f16_f32 v9, v8, v9
	v_cvt_pk_f16_f32 v8, v6, v7
	v_cvt_pk_f16_f32 v7, v4, v5
	v_cvt_pk_f16_f32 v6, v2, v3
	v_cvt_pk_f16_f32 v5, v16, v17
	v_cvt_pk_f16_f32 v4, v14, v15
	s_waitcnt vmcnt(1) lgkmcnt(1)
	v_mfma_f32_32x32x16_f16 v[50:65], v[26:29], v[30:33], v[50:65]
	global_load_dwordx4 v[30:33], v168, s[2:3]
	global_load_dwordx4 v[86:89], v[152:153], off offset:1024
	s_nop 0
	global_load_dwordx4 v[168:171], v168, s[0:1]
	v_cvt_pk_f16_f32 v3, v12, v13
	v_cvt_pk_f16_f32 v2, v10, v11
	ds_write_b128 v175, v[6:9]
	ds_write_b128 v174, v[2:5]
	v_cvt_pk_f16_f32 v5, v40, v41
	s_waitcnt vmcnt(3) lgkmcnt(2)
	v_mfma_f32_32x32x16_f16 v[50:65], v[82:85], v[66:69], v[50:65]
	global_load_dwordx4 v[182:185], v154, s[0:1] offset:1024
	v_cvt_pk_f16_f32 v4, v38, v39
	v_cvt_pk_f16_f32 v3, v36, v37
	v_cvt_pk_f16_f32 v2, v34, v35
	ds_write_b128 v175, v[2:5] offset:32768
	v_cvt_pk_f16_f32 v5, v48, v49
	v_cvt_pk_f16_f32 v4, v46, v47
	s_waitcnt vmcnt(3)
	v_mfma_f32_32x32x16_f16 v[66:81], v[18:21], v[30:33], 0
	global_load_dwordx4 v[18:21], v[152:153], off offset:2048
	v_cvt_pk_f16_f32 v3, v44, v45
	v_cvt_pk_f16_f32 v2, v42, v43
	ds_write_b128 v174, v[2:5] offset:32768
	v_cvt_pk_f16_f32 v57, v56, v57
	v_cvt_pk_f16_f32 v56, v54, v55
	v_cvt_pk_f16_f32 v55, v52, v53
	s_waitcnt vmcnt(3)
	v_mfma_f32_32x32x16_f16 v[66:81], v[22:25], v[86:89], v[66:81]
	global_load_dwordx4 v[22:25], v[152:153], off offset:3072
	v_cvt_pk_f16_f32 v54, v50, v51
	s_waitcnt vmcnt(1)
	v_mfma_f32_32x32x16_f16 v[66:81], v[26:29], v[18:21], v[66:81]
	v_lshl_add_u64 v[18:19], s[0:1], 0, v[154:155]
	v_add_co_u32_e32 v152, vcc, s23, v18
	s_nop 1
	v_addc_co_u32_e32 v153, vcc, 0, v19, vcc
	global_load_dwordx4 v[86:89], v[152:153], off offset:1024
	s_waitcnt vmcnt(1)
	v_mfma_f32_32x32x16_f16 v[66:81], v[82:85], v[22:25], v[66:81]
	v_cvt_pk_f16_f32 v85, v64, v65
	v_cvt_pk_f16_f32 v84, v62, v63
	v_cvt_pk_f16_f32 v83, v60, v61
	v_cvt_pk_f16_f32 v82, v58, v59
	v_mfma_f32_32x32x16_f16 v[18:33], v[54:57], v[126:129], 0
	s_nop 6
	v_cvt_pk_f16_f32 v73, v72, v73
	v_cvt_pk_f16_f32 v72, v70, v71
	v_cvt_pk_f16_f32 v70, v66, v67
	v_cvt_pk_f16_f32 v67, v76, v77
	v_cvt_pk_f16_f32 v66, v74, v75
	global_load_dwordx4 v[74:77], v154, s[0:1]
	ds_read_b128 v[2:5], v181
	ds_read_b128 v[6:9], v177
	ds_read_b128 v[10:13], v181 offset:32768
	global_load_dwordx4 v[14:17], v154, s[0:1] offset:2048
	global_load_dwordx4 v[34:37], v154, s[0:1] offset:3072
	v_mfma_f32_32x32x16_f16 v[50:65], v[54:57], v[110:113], 0
	v_cvt_pk_f16_f32 v71, v68, v69
	v_cvt_pk_f16_f32 v69, v80, v81
	v_cvt_pk_f16_f32 v68, v78, v79
	v_mfma_f32_32x32x16_f16 v[18:33], v[82:85], v[122:125], v[18:33]
	v_mfma_f32_32x32x16_f16 v[50:65], v[82:85], v[106:109], v[50:65]
	ds_read_b128 v[82:85], v177 offset:32768
	v_mfma_f32_32x32x16_f16 v[18:33], v[70:73], v[118:121], v[18:33]
	v_mfma_f32_32x32x16_f16 v[50:65], v[70:73], v[94:97], v[50:65]
	v_mfma_f32_32x32x16_f16 v[18:33], v[66:69], v[114:117], v[18:33]
	v_mfma_f32_32x32x16_f16 v[50:65], v[66:69], v[90:93], v[50:65]
	s_nop 10
	v_cvt_pk_f16_f32 v25, v24, v25
	v_cvt_pk_f16_f32 v24, v22, v23
	v_cvt_pk_f16_f32 v23, v20, v21
	v_cvt_pk_f16_f32 v22, v18, v19
	ds_write_b128 v132, v[22:25]
	s_waitcnt vmcnt(2) lgkmcnt(4)
	v_mfma_f32_32x32x16_f16 v[66:81], v[2:5], v[74:77], 0
	s_waitcnt lgkmcnt(3)
	v_mfma_f32_32x32x16_f16 v[66:81], v[6:9], v[182:185], v[66:81]
	s_waitcnt vmcnt(1) lgkmcnt(2)
	v_mfma_f32_32x32x16_f16 v[66:81], v[10:13], v[14:17], v[66:81]
	s_waitcnt vmcnt(0) lgkmcnt(1)
	v_mfma_f32_32x32x16_f16 v[66:81], v[82:85], v[34:37], v[66:81]
	v_mfma_f32_32x32x16_f16 v[34:49], v[2:5], v[168:171], 0
	global_load_dwordx4 v[2:5], v[152:153], off offset:2048
	s_nop 9
	v_cvt_pk_f16_f32 v73, v72, v73
	v_cvt_pk_f16_f32 v72, v70, v71
	v_cvt_pk_f16_f32 v71, v68, v69
	v_cvt_pk_f16_f32 v70, v66, v67
	v_cvt_pk_f16_f32 v69, v80, v81
	v_cvt_pk_f16_f32 v68, v78, v79
	v_mfma_f32_32x32x16_f16 v[34:49], v[6:9], v[86:89], v[34:49]
	global_load_dwordx4 v[6:9], v[152:153], off offset:3072
	v_cvt_pk_f16_f32 v67, v76, v77
	v_cvt_pk_f16_f32 v66, v74, v75
	s_waitcnt vmcnt(1)
	v_mfma_f32_32x32x16_f16 v[34:49], v[10:13], v[2:5], v[34:49]
	s_waitcnt vmcnt(0)
	v_mfma_f32_32x32x16_f16 v[34:49], v[82:85], v[6:9], v[34:49]
	v_mfma_f32_32x32x16_f16 v[2:17], v[70:73], v[126:129], 0
	s_nop 10
	v_cvt_pk_f16_f32 v41, v40, v41
	v_cvt_pk_f16_f32 v40, v38, v39
	v_cvt_pk_f16_f32 v38, v34, v35
	v_cvt_pk_f16_f32 v35, v44, v45
	v_cvt_pk_f16_f32 v34, v42, v43
	v_cvt_pk_f16_f32 v45, v32, v33
	v_cvt_pk_f16_f32 v44, v30, v31
	v_cvt_pk_f16_f32 v43, v28, v29
	v_cvt_pk_f16_f32 v42, v26, v27
	v_mfma_f32_32x32x16_f16 v[18:33], v[70:73], v[110:113], 0
	v_cvt_pk_f16_f32 v39, v36, v37
	v_cvt_pk_f16_f32 v37, v48, v49
	v_cvt_pk_f16_f32 v36, v46, v47
	ds_write_b128 v131, v[42:45]
	v_cvt_pk_f16_f32 v45, v56, v57
	v_cvt_pk_f16_f32 v44, v54, v55
	v_cvt_pk_f16_f32 v43, v52, v53
	v_mfma_f32_32x32x16_f16 v[2:17], v[66:69], v[122:125], v[2:17]
	v_cvt_pk_f16_f32 v42, v50, v51
	ds_write_b128 v132, v[42:45] offset:32768
	v_cvt_pk_f16_f32 v45, v64, v65
	v_cvt_pk_f16_f32 v44, v62, v63
	v_cvt_pk_f16_f32 v43, v60, v61
	v_cvt_pk_f16_f32 v42, v58, v59
	ds_write_b128 v131, v[42:45] offset:32768
	v_mfma_f32_32x32x16_f16 v[18:33], v[66:69], v[106:109], v[18:33]
	v_mfma_f32_32x32x16_f16 v[2:17], v[38:41], v[118:121], v[2:17]
	v_mfma_f32_32x32x16_f16 v[18:33], v[38:41], v[94:97], v[18:33]
	v_mfma_f32_32x32x16_f16 v[2:17], v[34:37], v[114:117], v[2:17]
	v_mfma_f32_32x32x16_f16 v[18:33], v[34:37], v[90:93], v[18:33]
	s_nop 10
	v_cvt_pk_f16_f32 v9, v8, v9
	v_cvt_pk_f16_f32 v8, v6, v7
	v_cvt_pk_f16_f32 v7, v4, v5
	v_cvt_pk_f16_f32 v6, v2, v3
	v_cvt_pk_f16_f32 v5, v16, v17
	v_cvt_pk_f16_f32 v4, v14, v15
	v_cvt_pk_f16_f32 v3, v12, v13
	v_cvt_pk_f16_f32 v2, v10, v11
	ds_write_b128 v135, v[6:9]
	ds_write_b128 v133, v[2:5]
	v_cvt_pk_f16_f32 v5, v24, v25
	v_cvt_pk_f16_f32 v4, v22, v23
	v_cvt_pk_f16_f32 v3, v20, v21
	v_cvt_pk_f16_f32 v2, v18, v19
	ds_write_b128 v135, v[2:5] offset:32768
	v_cvt_pk_f16_f32 v5, v32, v33
	v_cvt_pk_f16_f32 v4, v30, v31
	v_cvt_pk_f16_f32 v3, v28, v29
	v_cvt_pk_f16_f32 v2, v26, v27
	ds_write_b128 v133, v[2:5] offset:32768
	s_setprio 0
	s_waitcnt lgkmcnt(0)
	s_barrier
	ds_read_b64_tr_b16 v[2:3], v146
	ds_read_b64_tr_b16 v[4:5], v147
	ds_read_b64_tr_b16 v[36:37], v147 offset:32768
	ds_read_b64_tr_b16 v[34:35], v146 offset:32768
	ds_read_b64_tr_b16 v[18:19], v150
	ds_read_b64_tr_b16 v[20:21], v151
	ds_read_b64_tr_b16 v[40:41], v151 offset:32768
	ds_read_b64_tr_b16 v[38:39], v150 offset:32768
	s_waitcnt lgkmcnt(6)
	v_mfma_f32_32x32x16_f16 v[2:17], v[2:5], v[102:105], 0
	ds_read_b64_tr_b16 v[42:43], v148
	ds_read_b64_tr_b16 v[44:45], v149
	ds_read_b64_tr_b16 v[48:49], v149 offset:32768
	ds_read_b64_tr_b16 v[46:47], v148 offset:32768
	v_cmp_gt_u32_e64 s[0:1], 32, v167
	s_cmp_eq_u32 s5, 0
	v_cmp_lt_i32_e64 s[2:3], v162, v163
	s_waitcnt lgkmcnt(6)
	v_mfma_f32_32x32x16_f16 v[18:33], v[18:21], v[102:105], 0
	v_mfma_f32_32x32x16_f16 v[2:17], v[34:37], v[98:101], v[2:17]
	s_waitcnt lgkmcnt(4)
	v_mfma_f32_32x32x16_f16 v[18:33], v[38:41], v[98:101], v[18:33]
	s_nop 9
	v_mul_f32_e64 v34, v16, v16
	v_mul_f32_e64 v35, v17, v17
	v_mul_f32_e64 v36, v12, v12
	v_mul_f32_e64 v37, v13, v13
	v_mul_f32_e64 v50, v8, v8
	v_mul_f32_e64 v51, v9, v9
	v_pk_mul_f32 v[52:53], v[4:5], v[4:5]
	v_pk_fma_f32 v[50:51], v[6:7], v[6:7], v[50:51]
	v_pk_fma_f32 v[52:53], v[2:3], v[2:3], v[52:53]
	v_pk_fma_f32 v[36:37], v[10:11], v[10:11], v[36:37]
	v_pk_fma_f32 v[34:35], v[14:15], v[14:15], v[34:35]
	v_pk_mul_f32 v[116:117], v[24:25], v[24:25]
	v_pk_mul_f32 v[118:119], v[20:21], v[20:21]
	v_pk_add_f32 v[50:51], v[52:53], v[50:51]
	v_pk_add_f32 v[34:35], v[36:37], v[34:35]
	v_pk_mul_f32 v[112:113], v[32:33], v[32:33]
	v_pk_mul_f32 v[114:115], v[28:29], v[28:29]
	v_pk_mul_f32 v[120:121], v[18:19], v[18:19]
	v_pk_fma_f32 v[18:19], v[18:19], v[18:19], v[118:119]
	v_pk_fma_f32 v[20:21], v[22:23], v[22:23], v[116:117]
	v_pk_add_f32 v[34:35], v[50:51], v[34:35]
	v_pk_mul_f32 v[106:107], v[22:23], v[22:23]
	v_pk_add_f32 v[18:19], v[18:19], v[20:21]
	v_pk_fma_f32 v[20:21], v[26:27], v[26:27], v[114:115]
	v_pk_fma_f32 v[22:23], v[30:31], v[30:31], v[112:113]
	v_add_f32_e32 v34, v34, v35
	v_pk_add_f32 v[20:21], v[20:21], v[22:23]
	v_add_f32_e32 v36, 0, v34
	v_pk_mul_f32 v[108:109], v[26:27], v[26:27]
	v_pk_mul_f32 v[110:111], v[30:31], v[30:31]
	v_pk_add_f32 v[34:35], v[18:19], v[20:21]
	s_waitcnt lgkmcnt(2)
	v_mfma_f32_32x32x16_f16 v[18:33], v[42:45], v[102:105], 0
	v_add_f32_e32 v34, v34, v35
	v_add_f32_e32 v54, v36, v34
	v_sub_f32_e32 v55, v36, v34
	ds_read_b64_tr_b16 v[34:35], v144
	ds_read_b64_tr_b16 v[36:37], v145
	ds_read_b64_tr_b16 v[52:53], v145 offset:32768
	ds_read_b64_tr_b16 v[50:51], v144 offset:32768
	v_pk_fma_f32 v[4:5], v[4:5], v[4:5], v[118:119]
	v_pk_fma_f32 v[16:17], v[16:17], v[16:17], v[112:113]
	v_pk_fma_f32 v[14:15], v[14:15], v[14:15], v[110:111]
	s_waitcnt lgkmcnt(4)
	v_mfma_f32_32x32x16_f16 v[18:33], v[46:49], v[98:101], v[18:33]
	v_fma_f32 v12, v12, v12, v114
	v_fma_f32 v13, v13, v13, v115
	v_fma_f32 v10, v10, v10, v108
	v_fma_f32 v11, v11, v11, v109
	v_fma_f32 v8, v8, v8, v116
	v_fma_f32 v9, v9, v9, v117
	v_pk_fma_f32 v[6:7], v[6:7], v[6:7], v[106:107]
	v_pk_fma_f32 v[2:3], v[2:3], v[2:3], v[120:121]
	s_nop 3
	v_pk_mul_f32 v[38:39], v[32:33], v[32:33]
	v_pk_mul_f32 v[40:41], v[28:29], v[28:29]
	v_pk_mul_f32 v[42:43], v[24:25], v[24:25]
	v_pk_mul_f32 v[44:45], v[20:21], v[20:21]
	v_pk_fma_f32 v[42:43], v[22:23], v[22:23], v[42:43]
	v_pk_fma_f32 v[44:45], v[18:19], v[18:19], v[44:45]
	v_pk_fma_f32 v[40:41], v[26:27], v[26:27], v[40:41]
	v_pk_fma_f32 v[38:39], v[30:31], v[30:31], v[38:39]
	v_pk_add_f32 v[42:43], v[44:45], v[42:43]
	v_pk_add_f32 v[38:39], v[40:41], v[38:39]
	v_pk_fma_f32 v[4:5], v[20:21], v[20:21], v[4:5]
	v_pk_add_f32 v[38:39], v[42:43], v[38:39]
	v_pk_fma_f32 v[6:7], v[22:23], v[22:23], v[6:7]
	v_add_f32_e32 v56, v38, v39
	s_waitcnt lgkmcnt(2)
	v_mfma_f32_32x32x16_f16 v[34:49], v[34:37], v[102:105], 0
	v_add_f32_e32 v70, v54, v56
	v_add_f32_e32 v71, v55, v56
	v_sub_f32_e32 v72, v54, v56
	ds_read_b64_tr_b16 v[54:55], v142
	ds_read_b64_tr_b16 v[56:57], v143
	ds_read_b64_tr_b16 v[68:69], v143 offset:32768
	ds_read_b64_tr_b16 v[66:67], v142 offset:32768
	v_pk_fma_f32 v[8:9], v[24:25], v[24:25], v[8:9]
	v_pk_fma_f32 v[10:11], v[26:27], v[26:27], v[10:11]
	v_pk_fma_f32 v[12:13], v[28:29], v[28:29], v[12:13]
	s_waitcnt lgkmcnt(4)
	v_mfma_f32_32x32x16_f16 v[34:49], v[50:53], v[98:101], v[34:49]
	v_fma_f32 v14, v30, v30, v14
	v_fma_f32 v15, v31, v31, v15
	v_fma_f32 v16, v32, v32, v16
	v_fma_f32 v17, v33, v33, v17
	v_fma_f32 v2, v18, v18, v2
	v_fma_f32 v3, v19, v19, v3
	s_nop 5
	v_pk_mul_f32 v[50:51], v[48:49], v[48:49]
	v_pk_mul_f32 v[52:53], v[44:45], v[44:45]
	v_pk_mul_f32 v[58:59], v[40:41], v[40:41]
	v_pk_mul_f32 v[60:61], v[36:37], v[36:37]
	v_pk_fma_f32 v[58:59], v[38:39], v[38:39], v[58:59]
	v_pk_fma_f32 v[60:61], v[34:35], v[34:35], v[60:61]
	v_pk_fma_f32 v[52:53], v[42:43], v[42:43], v[52:53]
	v_pk_fma_f32 v[50:51], v[46:47], v[46:47], v[50:51]
	v_pk_add_f32 v[58:59], v[60:61], v[58:59]
	v_pk_add_f32 v[50:51], v[52:53], v[50:51]
	v_pk_fma_f32 v[4:5], v[36:37], v[36:37], v[4:5]
	v_pk_add_f32 v[50:51], v[58:59], v[50:51]
	v_pk_fma_f32 v[16:17], v[48:49], v[48:49], v[16:17]
	v_add_f32_e32 v73, v50, v51
	s_waitcnt lgkmcnt(2)
	v_mfma_f32_32x32x16_f16 v[50:65], v[54:57], v[102:105], 0
	v_add_f32_e32 v86, v70, v73
	v_sub_f32_e32 v87, v71, v73
	v_sub_f32_e32 v88, v72, v73
	ds_read_b64_tr_b16 v[70:71], v140
	ds_read_b64_tr_b16 v[72:73], v141
	ds_read_b64_tr_b16 v[84:85], v141 offset:32768
	ds_read_b64_tr_b16 v[82:83], v140 offset:32768
	v_pk_fma_f32 v[14:15], v[46:47], v[46:47], v[14:15]
	v_pk_fma_f32 v[12:13], v[44:45], v[44:45], v[12:13]
	v_pk_fma_f32 v[10:11], v[42:43], v[42:43], v[10:11]
	s_waitcnt lgkmcnt(4)
	v_mfma_f32_32x32x16_f16 v[50:65], v[66:69], v[98:101], v[50:65]
	v_fma_f32 v8, v40, v40, v8
	v_fma_f32 v9, v41, v41, v9
	v_fma_f32 v6, v38, v38, v6
	v_fma_f32 v7, v39, v39, v7
	v_fma_f32 v2, v34, v34, v2
	v_fma_f32 v3, v35, v35, v3
	s_nop 5
	v_pk_mul_f32 v[66:67], v[64:65], v[64:65]
	v_pk_mul_f32 v[68:69], v[60:61], v[60:61]
	v_pk_mul_f32 v[74:75], v[56:57], v[56:57]
	v_pk_mul_f32 v[76:77], v[52:53], v[52:53]
	v_pk_fma_f32 v[74:75], v[54:55], v[54:55], v[74:75]
	v_pk_fma_f32 v[76:77], v[50:51], v[50:51], v[76:77]
	v_pk_fma_f32 v[68:69], v[58:59], v[58:59], v[68:69]
	v_pk_fma_f32 v[66:67], v[62:63], v[62:63], v[66:67]
	v_pk_add_f32 v[74:75], v[76:77], v[74:75]
	v_pk_add_f32 v[66:67], v[68:69], v[66:67]
	v_pk_fma_f32 v[4:5], v[52:53], v[52:53], v[4:5]
	v_pk_add_f32 v[66:67], v[74:75], v[66:67]
	v_pk_fma_f32 v[6:7], v[54:55], v[54:55], v[6:7]
	v_add_f32_e32 v89, v66, v67
	s_waitcnt lgkmcnt(2)
	v_mfma_f32_32x32x16_f16 v[66:81], v[70:73], v[102:105], 0
	v_add_f32_e32 v94, v86, v89
	v_add_f32_e32 v126, v87, v89
	v_add_f32_e32 v127, v88, v89
	v_sub_f32_e32 v128, v86, v89
	ds_read_b64_tr_b16 v[86:87], v138
	ds_read_b64_tr_b16 v[88:89], v139
	ds_read_b64_tr_b16 v[124:125], v139 offset:32768
	ds_read_b64_tr_b16 v[122:123], v138 offset:32768
	v_pk_fma_f32 v[8:9], v[56:57], v[56:57], v[8:9]
	v_pk_fma_f32 v[10:11], v[58:59], v[58:59], v[10:11]
	s_waitcnt lgkmcnt(4)
	v_mfma_f32_32x32x16_f16 v[66:81], v[82:85], v[98:101], v[66:81]
	v_fma_f32 v12, v60, v60, v12
	v_fma_f32 v13, v61, v61, v13
	v_fma_f32 v14, v62, v62, v14
	v_fma_f32 v15, v63, v63, v15
	v_fma_f32 v16, v64, v64, v16
	v_fma_f32 v17, v65, v65, v17
	v_pk_fma_f32 v[2:3], v[50:51], v[50:51], v[2:3]
	s_nop 4
	v_pk_mul_f32 v[82:83], v[80:81], v[80:81]
	v_pk_mul_f32 v[84:85], v[76:77], v[76:77]
	v_pk_mul_f32 v[90:91], v[72:73], v[72:73]
	v_pk_mul_f32 v[92:93], v[68:69], v[68:69]
	v_pk_fma_f32 v[90:91], v[70:71], v[70:71], v[90:91]
	v_pk_fma_f32 v[92:93], v[66:67], v[66:67], v[92:93]
	v_pk_fma_f32 v[84:85], v[74:75], v[74:75], v[84:85]
	v_pk_fma_f32 v[82:83], v[78:79], v[78:79], v[82:83]
	v_pk_add_f32 v[90:91], v[92:93], v[90:91]
	v_pk_add_f32 v[82:83], v[84:85], v[82:83]
	v_pk_fma_f32 v[4:5], v[68:69], v[68:69], v[4:5]
	v_pk_add_f32 v[82:83], v[90:91], v[82:83]
	v_pk_fma_f32 v[18:19], v[80:81], v[80:81], v[16:17]
	v_add_f32_e32 v129, v82, v83
	v_add_f32_e32 v131, v94, v129
	s_waitcnt lgkmcnt(2)
	v_mfma_f32_32x32x16_f16 v[82:97], v[86:89], v[102:105], 0
	v_sub_f32_e32 v135, v126, v129
	v_add_f32_e32 v142, v127, v129
	v_sub_f32_e32 v143, v128, v129
	ds_read_b64_tr_b16 v[126:127], v136
	ds_read_b64_tr_b16 v[128:129], v137
	ds_read_b64_tr_b16 v[138:139], v137 offset:32768
	ds_read_b64_tr_b16 v[136:137], v136 offset:32768
	v_pk_fma_f32 v[20:21], v[78:79], v[78:79], v[14:15]
	v_pk_fma_f32 v[22:23], v[76:77], v[76:77], v[12:13]
	v_pk_fma_f32 v[24:25], v[74:75], v[74:75], v[10:11]
	s_waitcnt lgkmcnt(4)
	v_mfma_f32_32x32x16_f16 v[82:97], v[122:125], v[98:101], v[82:97]
	v_fma_f32 v26, v72, v72, v8
	v_fma_f32 v27, v73, v73, v9
	v_fma_f32 v28, v70, v70, v6
	v_fma_f32 v29, v71, v71, v7
	v_fma_f32 v30, v66, v66, v2
	v_fma_f32 v31, v67, v67, v3
	s_nop 5
	v_pk_fma_f32 v[32:33], v[84:85], v[84:85], v[4:5]
	s_waitcnt lgkmcnt(2)
	v_mfma_f32_32x32x16_f16 v[2:17], v[126:129], v[102:105], 0
	v_fma_f32 v28, v86, v86, v28
	v_fma_f32 v29, v87, v87, v29
	v_fma_f32 v24, v90, v90, v24
	v_fma_f32 v25, v91, v91, v25
	v_fma_f32 v22, v92, v92, v22
	v_fma_f32 v23, v93, v93, v23
	v_pk_fma_f32 v[20:21], v[94:95], v[94:95], v[20:21]
	v_pk_fma_f32 v[18:19], v[96:97], v[96:97], v[18:19]
	v_pk_fma_f32 v[30:31], v[82:83], v[82:83], v[30:31]
	v_pk_fma_f32 v[26:27], v[88:89], v[88:89], v[26:27]
	s_waitcnt lgkmcnt(0)
	v_mfma_f32_32x32x16_f16 v[2:17], v[136:139], v[98:101], v[2:17]
	v_mul_f32_e64 v122, v96, v96
	v_mul_f32_e64 v123, v97, v97
	v_mul_f32_e64 v124, v92, v92
	v_mul_f32_e64 v125, v93, v93
	v_mul_f32_e64 v132, v88, v88
	v_mul_f32_e64 v133, v89, v89
	v_pk_mul_f32 v[140:141], v[84:85], v[84:85]
	v_pk_fma_f32 v[132:133], v[86:87], v[86:87], v[132:133]
	v_pk_fma_f32 v[140:141], v[82:83], v[82:83], v[140:141]
	v_pk_fma_f32 v[124:125], v[90:91], v[90:91], v[124:125]
	s_nop 1
	v_pk_mul_f32 v[38:39], v[8:9], v[8:9]
	v_pk_mul_f32 v[40:41], v[4:5], v[4:5]
	v_pk_mul_f32 v[34:35], v[16:17], v[16:17]
	v_pk_mul_f32 v[36:37], v[12:13], v[12:13]
	v_pk_fma_f32 v[16:17], v[16:17], v[16:17], v[18:19]
	v_pk_fma_f32 v[18:19], v[14:15], v[14:15], v[20:21]
	v_pk_fma_f32 v[12:13], v[12:13], v[12:13], v[22:23]
	v_pk_fma_f32 v[20:21], v[10:11], v[10:11], v[24:25]
	v_pk_fma_f32 v[22:23], v[6:7], v[6:7], v[28:29]
	v_pk_fma_f32 v[24:25], v[2:3], v[2:3], v[30:31]
	v_pk_fma_f32 v[2:3], v[2:3], v[2:3], v[40:41]
	v_pk_fma_f32 v[6:7], v[6:7], v[6:7], v[38:39]
	v_pk_fma_f32 v[4:5], v[4:5], v[4:5], v[32:33]
	v_pk_add_f32 v[2:3], v[2:3], v[6:7]
	v_pk_fma_f32 v[6:7], v[10:11], v[10:11], v[36:37]
	v_pk_fma_f32 v[10:11], v[14:15], v[14:15], v[34:35]
	v_pk_fma_f32 v[8:9], v[8:9], v[8:9], v[26:27]
	v_pk_add_f32 v[6:7], v[6:7], v[10:11]
	v_sub_f32_e32 v10, v24, v25
	v_add_f32_e32 v11, v25, v24
	v_add_f32_e32 v10, v4, v10
	v_sub_f32_e32 v14, v11, v4
	v_add_f32_e32 v4, v4, v11
	v_sub_f32_e32 v10, v10, v5
	v_sub_f32_e32 v11, v14, v5
	v_add_f32_e32 v4, v5, v4
	v_add_f32_e32 v5, v22, v10
	v_add_f32_e32 v10, v22, v11
	v_sub_f32_e32 v11, v4, v22
	v_add_f32_e32 v4, v22, v4
	v_sub_f32_e32 v5, v5, v23
	v_add_f32_e32 v10, v23, v10
	v_sub_f32_e32 v11, v11, v23
	v_add_f32_e32 v4, v23, v4
	v_add_f32_e32 v5, v8, v5
	v_sub_f32_e32 v10, v10, v8
	v_sub_f32_e32 v11, v11, v8
	v_add_f32_e32 v4, v8, v4
	v_sub_f32_e32 v5, v5, v9
	v_pk_fma_f32 v[122:123], v[94:95], v[94:95], v[122:123]
	v_sub_f32_e32 v8, v10, v9
	v_sub_f32_e32 v10, v11, v9
	v_add_f32_e32 v4, v9, v4
	v_add_f32_e32 v5, v20, v5
	v_pk_add_f32 v[132:133], v[140:141], v[132:133]
	v_pk_add_f32 v[122:123], v[124:125], v[122:123]
	v_add_f32_e32 v8, v20, v8
	v_add_f32_e32 v9, v20, v10
	v_sub_f32_e32 v4, v4, v20
	v_sub_f32_e32 v5, v5, v21
	v_pk_add_f32 v[122:123], v[132:133], v[122:123]
	v_add_f32_e32 v8, v21, v8
	v_add_f32_e32 v9, v21, v9
	v_sub_f32_e32 v4, v4, v21
	v_add_f32_e32 v5, v12, v5
	v_add_f32_e32 v122, v122, v123
	v_pk_add_f32 v[2:3], v[2:3], v[6:7]
	v_sub_f32_e32 v8, v8, v12
	v_add_f32_e32 v9, v12, v9
	v_sub_f32_e32 v4, v4, v12
	v_sub_f32_e32 v5, v5, v13
	v_add_f32_e32 v123, v131, v122
	v_add_f32_e32 v2, v2, v3
	v_sub_f32_e32 v8, v8, v13
	v_add_f32_e32 v9, v13, v9
	v_sub_f32_e32 v4, v4, v13
	v_add_f32_e32 v5, v18, v5
	v_add_f32_e32 v3, v123, v2
	v_add_f32_e32 v8, v18, v8
	v_sub_f32_e32 v9, v9, v18
	v_sub_f32_e32 v4, v4, v18
	v_sub_f32_e32 v5, v5, v19
	v_and_b32_e32 v10, 8, v156
	v_add_f32_e32 v8, v19, v8
	v_sub_f32_e32 v9, v9, v19
	v_sub_f32_e32 v4, v4, v19
	v_add_f32_e32 v5, v16, v5
	v_cmp_eq_u32_e32 vcc, 0, v10
	v_cndmask_b32_e64 v10, -v3, v3, s[0:1]
	s_cselect_b64 s[0:1], -1, 0
	s_bitcmp0_b32 s4, 7
	v_sub_f32_e32 v8, v8, v16
	v_sub_f32_e32 v9, v9, v16
	v_sub_f32_e32 v4, v4, v16
	v_sub_f32_e32 v5, v5, v17
	v_cndmask_b32_e64 v11, -v3, v3, s[0:1]
	s_cselect_b64 s[0:1], -1, 0
	v_and_b32_e32 v16, 32, v156
	v_sub_f32_e32 v8, v8, v17
	v_cndmask_b32_e64 v5, -v5, v5, vcc
	v_cndmask_b32_e64 v12, -v3, v3, s[0:1]
	v_cndmask_b32_e64 v18, v161, v162, s[2:3]
	v_cmp_eq_u32_e64 s[2:3], 0, v16
	v_lshlrev_b32_e32 v18, 2, v18
	v_cmp_eq_u32_e64 s[0:1], 0, v134
	v_cndmask_b32_e64 v16, v11, v5, s[2:3]
	v_cndmask_b32_e64 v5, v5, v11, s[2:3]
	v_cndmask_b32_e64 v11, v8, v12, s[2:3]
	ds_bpermute_b32 v11, v18, v11
	v_and_b32_e32 v14, 2, v156
	v_cndmask_b32_e64 v13, -v3, v3, s[0:1]
	v_cmp_eq_u32_e64 s[0:1], 0, v14
	v_cndmask_b32_e64 v8, v12, v8, s[2:3]
	v_add_f32_e32 v124, v135, v122
	v_cndmask_b32_e64 v14, -v3, v3, s[0:1]
	v_cmp_eq_u32_e64 s[0:1], 0, v130
	v_sub_f32_e32 v4, v4, v17
	s_waitcnt lgkmcnt(0)
	v_add_f32_e32 v8, v8, v11
	v_cndmask_b32_e64 v15, -v3, v3, s[0:1]
	v_cndmask_b32_e64 v11, v14, v10, s[2:3]
	v_cndmask_b32_e64 v10, v10, v14, s[2:3]
	v_sub_f32_e32 v6, v124, v2
	v_sub_f32_e32 v9, v9, v17
	v_cndmask_b32_e64 v3, -v3, v3, vcc
	ds_bpermute_b32 v10, v18, v10
	v_cndmask_b32_e64 v12, v4, v15, s[2:3]
	v_sub_f32_e32 v125, v142, v122
	v_cndmask_b32_e64 v19, v9, v13, s[2:3]
	v_cndmask_b32_e64 v9, v13, v9, s[2:3]
	ds_bpermute_b32 v12, v18, v12
	v_cndmask_b32_e64 v13, v6, v3, s[2:3]
	v_sub_f32_e32 v7, v125, v2
	v_bfe_i32 v17, v156, 5, 1
	ds_bpermute_b32 v5, v18, v5
	ds_bpermute_b32 v13, v18, v13
	v_sub_f32_e32 v122, v143, v122
	v_cndmask_b32_e64 v3, v3, v6, s[2:3]
	v_and_b32_e32 v6, v17, v7
	v_sub_f32_e32 v2, v122, v2
	ds_bpermute_b32 v19, v18, v19
	ds_bpermute_b32 v6, v18, v6
	s_waitcnt lgkmcnt(5)
	v_add_f32_e32 v10, v11, v10
	v_cndmask_b32_e64 v4, v15, v4, s[2:3]
	v_and_b32_e32 v11, v17, v2
	s_waitcnt lgkmcnt(4)
	v_add_f32_e32 v4, v4, v12
	ds_bpermute_b32 v11, v18, v11
	v_and_b32_e32 v12, 16, v156
	v_cmp_lt_i32_e64 s[4:5], v164, v163
	s_waitcnt lgkmcnt(4)
	v_add_f32_e32 v5, v16, v5
	s_waitcnt lgkmcnt(3)
	v_add_f32_e32 v3, v3, v13
	v_cndmask_b32_e64 v13, v161, v164, s[4:5]
	v_cmp_eq_u32_e64 s[4:5], 0, v12
	s_waitcnt lgkmcnt(2)
	v_add_f32_e32 v9, v9, v19
	v_lshlrev_b32_e32 v13, 2, v13
	v_cndmask_b32_e64 v12, v4, v5, s[4:5]
	v_cndmask_b32_e64 v4, v5, v4, s[4:5]
	v_cndmask_b32_e64 v5, 0, v7, s[2:3]
	s_waitcnt lgkmcnt(1)
	v_add_f32_e32 v5, v5, v6
	v_cndmask_b32_e64 v2, 0, v2, s[2:3]
	v_cndmask_b32_e64 v7, v9, v5, s[4:5]
	ds_bpermute_b32 v4, v13, v4
	s_waitcnt lgkmcnt(1)
	v_add_f32_e32 v2, v2, v11
	v_cndmask_b32_e64 v6, v3, v8, s[4:5]
	v_cndmask_b32_e64 v3, v8, v3, s[4:5]
	ds_bpermute_b32 v7, v13, v7
	ds_bpermute_b32 v3, v13, v3
	v_cndmask_b32_e64 v8, v10, v2, s[4:5]
	ds_bpermute_b32 v8, v13, v8
	v_cndmask_b32_e64 v5, v5, v9, s[4:5]
	s_waitcnt lgkmcnt(3)
	v_add_f32_e32 v4, v12, v4
	s_waitcnt lgkmcnt(2)
	v_add_f32_e32 v5, v5, v7
	s_waitcnt lgkmcnt(1)
	v_add_f32_e32 v3, v6, v3
	v_cndmask_b32_e64 v2, v2, v10, s[4:5]
	v_cndmask_b32_e32 v6, v5, v4, vcc
	v_cndmask_b32_e32 v4, v4, v5, vcc
	v_mov_b32_e32 v5, v155
	s_waitcnt lgkmcnt(0)
	v_add_f32_e32 v2, v2, v8
	v_mov_b32_dpp v5, v4 row_mirror row_mask:0xf bank_mask:0xf
	s_nop 1
	v_add_f32_dpp v4, v5, v6 row_half_mirror row_mask:0xf bank_mask:0xf bound_ctrl:1
	v_cndmask_b32_e32 v5, v2, v3, vcc
	v_cndmask_b32_e32 v2, v3, v2, vcc
	v_mov_b32_e32 v3, v155
	s_nop 1
	v_mov_b32_dpp v3, v2 row_mirror row_mask:0xf bank_mask:0xf
	s_nop 1
	v_add_f32_dpp v2, v3, v5 row_half_mirror row_mask:0xf bank_mask:0xf bound_ctrl:1
	v_cndmask_b32_e64 v3, v2, v4, s[0:1]
	v_cndmask_b32_e64 v2, v4, v2, s[0:1]
	v_mov_b32_e32 v4, v155
	s_nop 1
	v_mov_b32_dpp v4, v2 row_half_mirror row_mask:0xf bank_mask:0xf
	s_nop 1
	v_add_f32_dpp v2, v4, v3 quad_perm:[3,2,1,0] row_mask:0xf bank_mask:0xf bound_ctrl:1
	v_and_b32_e32 v4, 3, v156
	v_cmp_eq_u32_e32 vcc, 0, v4
	v_and_b32_e32 v4, 56, v156
	v_add_f32_dpp v2, v2, v2 quad_perm:[2,3,0,1] row_mask:0xf bank_mask:0xf bound_ctrl:1
	v_mov_b32_e32 v3, 0
	v_cmp_ne_u32_e64 s[0:1], 56, v4
	s_and_b64 s[2:3], vcc, s[0:1]
	v_mov_b32_dpp v3, v2 quad_perm:[1,0,3,2] row_mask:0xf bank_mask:0xf
	s_and_saveexec_b64 s[0:1], s[2:3]
	v_and_b32_e32 v4, 0xfc, v156
	v_add_f32_e32 v2, v2, v3
	v_or_b32_e32 v4, v165, v4
	ds_write_b32 v4, v2
	s_or_b64 exec, exec, s[0:1]
	v_cmp_gt_i32_e32 vcc, 14, v156
	s_waitcnt lgkmcnt(0)
	s_barrier
	s_and_saveexec_b64 s[0:1], vcc
	s_cbranch_execz .LBB1_2
	ds_read_b32 v2, v166
	ds_read_b32 v3, v166 offset:64
	ds_read_b32 v4, v166 offset:128
	ds_read_b32 v5, v166 offset:192
	s_waitcnt lgkmcnt(2)
	v_add_f32_e32 v2, v2, v3
	s_waitcnt lgkmcnt(1)
	v_add_f32_e32 v2, v2, v4
	s_waitcnt lgkmcnt(0)
	v_add_f32_e32 v2, v2, v5
	v_mul_f32_e32 v4, 0x39800000, v2
	v_lshl_add_u64 v[2:3], v[156:157], 2, s[14:15]
	global_store_dword v[2:3], v4, off
	s_branch .LBB1_2
